# GEMM K-loops: no per-phase s_setprio flips and no duplicate lgkmcnt(0) behind the phase barrier (on top of the guarded GQA fast softmax)
# speedup vs baseline: 1.0082x; 1.0082x over previous
.LBB0_514:
	s_add_u32 s22, s82, s92
	s_addc_u32 s23, s83, s93
	s_add_u32 s24, s22, 0x100
	s_addc_u32 s25, s23, 0
	s_add_u32 s58, s3, s92
	s_addc_u32 s59, s2, s93
	s_add_i32 vcc_lo, 0, 0x10000
	s_cmpk_eq_i32 s92, 0xf00
	s_cselect_b64 s[26:27], -1, 0
	s_and_b64 s[22:23], s[26:27], exec
	s_cselect_b32 s25, s67, s25
	s_cselect_b32 s24, s75, s24
	s_cselect_b32 s23, s95, s59
	s_cselect_b32 s22, s29, s58
	s_add_i32 vcc_hi, 0, 0x14000
	v_add_u32_e32 v130, vcc_lo, v223
	v_add_u32_e32 v142, vcc_hi, v223
	ds_read_b128 v[146:149], v130
	ds_read_b128 v[150:153], v130 offset:1024
	ds_read_b128 v[154:157], v130 offset:2048
	ds_read_b128 v[158:161], v130 offset:3072
	ds_read_b128 v[130:133], v142
	ds_read_b128 v[134:137], v142 offset:1024
	ds_read_b128 v[138:141], v142 offset:2048
	ds_read_b128 v[142:145], v142 offset:3072
	v_lshl_add_u64 v[214:215], v[210:211], 0, s[92:93]
	s_add_i32 m0, s81, 0xc000
	s_waitcnt lgkmcnt(0)
	ds_read_b128 v[162:165], v224
	ds_read_b128 v[166:169], v224 offset:1024
	ds_read_b128 v[170:173], v224 offset:2048
	ds_read_b128 v[174:177], v224 offset:3072
	ds_read_b128 v[178:181], v224 offset:4096
	ds_read_b128 v[182:185], v224 offset:5120
	ds_read_b128 v[186:189], v224 offset:6144
	ds_read_b128 v[190:193], v224 offset:7168
	global_load_lds_dwordx4 v[214:215], off
	v_lshl_add_u64 v[214:215], v[212:213], 0, s[92:93]
	s_add_i32 m0, s81, 0xe000
	s_nop 0
	global_load_lds_dwordx4 v[214:215], off
	s_waitcnt vmcnt(8)
	s_waitcnt lgkmcnt(0)
	s_barrier
	v_mfma_f32_16x16x32_bf16 v[124:127], v[146:149], v[162:165], v[124:127]
	v_mfma_f32_16x16x32_bf16 v[120:123], v[154:157], v[162:165], v[120:123]
	v_mfma_f32_16x16x32_bf16 v[116:119], v[146:149], v[170:173], v[116:119]
	v_mfma_f32_16x16x32_bf16 v[108:111], v[154:157], v[170:173], v[108:111]
	v_mfma_f32_16x16x32_bf16 v[100:103], v[146:149], v[178:181], v[100:103]
	v_mfma_f32_16x16x32_bf16 v[92:95], v[154:157], v[178:181], v[92:95]
	v_mfma_f32_16x16x32_bf16 v[84:87], v[146:149], v[186:189], v[84:87]
	v_mfma_f32_16x16x32_bf16 v[76:79], v[154:157], v[186:189], v[76:79]
	v_mfma_f32_16x16x32_bf16 v[124:127], v[150:153], v[166:169], v[124:127]
	v_mfma_f32_16x16x32_bf16 v[120:123], v[158:161], v[166:169], v[120:123]
	v_mfma_f32_16x16x32_bf16 v[116:119], v[150:153], v[174:177], v[116:119]
	v_mfma_f32_16x16x32_bf16 v[108:111], v[158:161], v[174:177], v[108:111]
	v_mfma_f32_16x16x32_bf16 v[100:103], v[150:153], v[182:185], v[100:103]
	v_mfma_f32_16x16x32_bf16 v[92:95], v[158:161], v[182:185], v[92:95]
	v_mfma_f32_16x16x32_bf16 v[84:87], v[150:153], v[190:193], v[84:87]
	v_mfma_f32_16x16x32_bf16 v[76:79], v[158:161], v[190:193], v[76:79]
	v_mfma_f32_16x16x32_bf16 v[112:115], v[130:133], v[162:165], v[112:115]
	v_mfma_f32_16x16x32_bf16 v[104:107], v[138:141], v[162:165], v[104:107]
	v_mfma_f32_16x16x32_bf16 v[96:99], v[130:133], v[170:173], v[96:99]
	v_mfma_f32_16x16x32_bf16 v[88:91], v[138:141], v[170:173], v[88:91]
	v_mfma_f32_16x16x32_bf16 v[80:83], v[130:133], v[178:181], v[80:83]
	v_mfma_f32_16x16x32_bf16 v[72:75], v[138:141], v[178:181], v[72:75]
	v_mfma_f32_16x16x32_bf16 v[68:71], v[130:133], v[186:189], v[68:71]
	v_mfma_f32_16x16x32_bf16 v[64:67], v[138:141], v[186:189], v[64:67]
	v_mfma_f32_16x16x32_bf16 v[112:115], v[134:137], v[166:169], v[112:115]
	v_mfma_f32_16x16x32_bf16 v[104:107], v[142:145], v[166:169], v[104:107]
	v_mfma_f32_16x16x32_bf16 v[96:99], v[134:137], v[174:177], v[96:99]
	v_mfma_f32_16x16x32_bf16 v[88:91], v[142:145], v[174:177], v[88:91]
	v_mfma_f32_16x16x32_bf16 v[80:83], v[134:137], v[182:185], v[80:83]
	v_mfma_f32_16x16x32_bf16 v[72:75], v[142:145], v[182:185], v[72:75]
	v_mfma_f32_16x16x32_bf16 v[68:71], v[134:137], v[190:193], v[68:71]
	v_mfma_f32_16x16x32_bf16 v[64:67], v[142:145], v[190:193], v[64:67]
	s_barrier
	s_add_i32 s58, vcc_lo, s28
	v_lshl_add_u64 v[214:215], s[22:23], 0, v[200:201]
	s_mov_b32 m0, s58
	ds_read_b128 v[186:189], v224 offset:16384
	ds_read_b128 v[190:193], v224 offset:17408
	ds_read_b128 v[178:181], v224 offset:18432
	ds_read_b128 v[182:185], v224 offset:19456
	ds_read_b128 v[170:173], v224 offset:20480
	ds_read_b128 v[174:177], v224 offset:21504
	ds_read_b128 v[162:165], v224 offset:22528
	ds_read_b128 v[166:169], v224 offset:23552
	global_load_lds_dwordx4 v[214:215], off
	s_add_i32 m0, s58, 0x2000
	s_add_u32 s58, s22, 0x80000
	v_lshl_add_u64 v[216:217], s[22:23], 0, v[204:205]
	s_addc_u32 s59, s23, 0
	s_add_i32 vcc_lo, vcc_hi, s28
	global_load_lds_dwordx4 v[216:217], off
	v_lshl_add_u64 v[218:219], s[58:59], 0, v[200:201]
	s_mov_b32 m0, vcc_lo
	v_lshl_add_u64 v[220:221], s[24:25], 0, v[202:203]
	global_load_lds_dwordx4 v[218:219], off
	v_lshl_add_u64 v[218:219], s[58:59], 0, v[204:205]
	s_add_i32 m0, vcc_lo, 0x2000
	v_cndmask_b32_e64 v194, 0, 1, s[96:97]
	global_load_lds_dwordx4 v[218:219], off
	v_lshl_add_u64 v[218:219], s[24:25], 0, v[198:199]
	s_mov_b32 m0, s81
	v_cmp_ne_u32_e64 s[58:59], 1, v194
	global_load_lds_dwordx4 v[218:219], off
	s_mov_b32 m0, s88
	s_andn2_b64 vcc, exec, s[96:97]
	global_load_lds_dwordx4 v[220:221], off
	s_waitcnt vmcnt(8)
	s_waitcnt lgkmcnt(0)
	s_barrier
	s_cbranch_vccnz .LBB0_516
	s_waitcnt lgkmcnt(0)
	v_mfma_f32_16x16x32_bf16 v[60:63], v[146:149], v[186:189], v[60:63]
	v_mfma_f32_16x16x32_bf16 v[56:59], v[154:157], v[186:189], v[56:59]
	v_mfma_f32_16x16x32_bf16 v[44:47], v[146:149], v[178:181], v[44:47]
	v_mfma_f32_16x16x32_bf16 v[40:43], v[154:157], v[178:181], v[40:43]
	v_mfma_f32_16x16x32_bf16 v[28:31], v[146:149], v[170:173], v[28:31]
	v_mfma_f32_16x16x32_bf16 v[24:27], v[154:157], v[170:173], v[24:27]
	v_mfma_f32_16x16x32_bf16 v[12:15], v[146:149], v[162:165], v[12:15]
	v_mfma_f32_16x16x32_bf16 v[8:11], v[154:157], v[162:165], v[8:11]
	v_mfma_f32_16x16x32_bf16 v[60:63], v[150:153], v[190:193], v[60:63]
	v_mfma_f32_16x16x32_bf16 v[56:59], v[158:161], v[190:193], v[56:59]
	v_mfma_f32_16x16x32_bf16 v[44:47], v[150:153], v[182:185], v[44:47]
	v_mfma_f32_16x16x32_bf16 v[40:43], v[158:161], v[182:185], v[40:43]
	v_mfma_f32_16x16x32_bf16 v[28:31], v[150:153], v[174:177], v[28:31]
	v_mfma_f32_16x16x32_bf16 v[24:27], v[158:161], v[174:177], v[24:27]
	v_mfma_f32_16x16x32_bf16 v[12:15], v[150:153], v[166:169], v[12:15]
	v_mfma_f32_16x16x32_bf16 v[8:11], v[158:161], v[166:169], v[8:11]
	v_mfma_f32_16x16x32_bf16 v[52:55], v[130:133], v[186:189], v[52:55]
	v_mfma_f32_16x16x32_bf16 v[48:51], v[138:141], v[186:189], v[48:51]
	v_mfma_f32_16x16x32_bf16 v[36:39], v[130:133], v[178:181], v[36:39]
	v_mfma_f32_16x16x32_bf16 v[32:35], v[138:141], v[178:181], v[32:35]
	v_mfma_f32_16x16x32_bf16 v[20:23], v[130:133], v[170:173], v[20:23]
	v_mfma_f32_16x16x32_bf16 v[16:19], v[138:141], v[170:173], v[16:19]
	v_mfma_f32_16x16x32_bf16 v[4:7], v[130:133], v[162:165], v[4:7]
	v_mfma_f32_16x16x32_bf16 v[0:3], v[138:141], v[162:165], v[0:3]
	v_mfma_f32_16x16x32_bf16 v[52:55], v[134:137], v[190:193], v[52:55]
	v_mfma_f32_16x16x32_bf16 v[48:51], v[142:145], v[190:193], v[48:51]
	v_mfma_f32_16x16x32_bf16 v[36:39], v[134:137], v[182:185], v[36:39]
	v_mfma_f32_16x16x32_bf16 v[32:35], v[142:145], v[182:185], v[32:35]
	v_mfma_f32_16x16x32_bf16 v[20:23], v[134:137], v[174:177], v[20:23]
	v_mfma_f32_16x16x32_bf16 v[16:19], v[142:145], v[174:177], v[16:19]
	v_mfma_f32_16x16x32_bf16 v[4:7], v[134:137], v[166:169], v[4:7]
	v_mfma_f32_16x16x32_bf16 v[0:3], v[142:145], v[166:169], v[0:3]
.LBB0_516:
	s_barrier
	s_add_i32 vcc_lo, 0, 0x18000
	s_add_i32 vcc_hi, 0, 0x1c000
	v_add_u32_e32 v130, vcc_lo, v223
	v_add_u32_e32 v142, vcc_hi, v223
	ds_read_b128 v[146:149], v130
	ds_read_b128 v[150:153], v130 offset:1024
	ds_read_b128 v[154:157], v130 offset:2048
	ds_read_b128 v[158:161], v130 offset:3072
	ds_read_b128 v[130:133], v142
	ds_read_b128 v[134:137], v142 offset:1024
	ds_read_b128 v[138:141], v142 offset:2048
	ds_read_b128 v[142:145], v142 offset:3072
	s_and_b64 s[26:27], s[26:27], exec
	s_cselect_b32 s27, s72, s86
	s_cselect_b32 s26, 0, s87
	s_add_u32 s24, s24, s27
	s_addc_u32 s25, s25, s26
	s_mov_b32 m0, s89
	v_lshl_add_u64 v[226:227], s[24:25], 0, v[198:199]
	s_waitcnt lgkmcnt(0)
	ds_read_b128 v[162:165], v224 offset:32768
	ds_read_b128 v[166:169], v224 offset:33792
	ds_read_b128 v[170:173], v224 offset:34816
	ds_read_b128 v[174:177], v224 offset:35840
	ds_read_b128 v[178:181], v224 offset:36864
	ds_read_b128 v[182:185], v224 offset:37888
	ds_read_b128 v[186:189], v224 offset:38912
	ds_read_b128 v[190:193], v224 offset:39936
	global_load_lds_dwordx4 v[226:227], off
	v_lshl_add_u64 v[226:227], s[24:25], 0, v[202:203]
	s_mov_b32 m0, s90
	s_nop 0
	global_load_lds_dwordx4 v[226:227], off
	s_waitcnt vmcnt(8)
	s_waitcnt lgkmcnt(0)
	s_barrier
	v_mfma_f32_16x16x32_bf16 v[124:127], v[146:149], v[162:165], v[124:127]
	v_mfma_f32_16x16x32_bf16 v[120:123], v[154:157], v[162:165], v[120:123]
	v_mfma_f32_16x16x32_bf16 v[116:119], v[146:149], v[170:173], v[116:119]
	v_mfma_f32_16x16x32_bf16 v[108:111], v[154:157], v[170:173], v[108:111]
	v_mfma_f32_16x16x32_bf16 v[100:103], v[146:149], v[178:181], v[100:103]
	v_mfma_f32_16x16x32_bf16 v[92:95], v[154:157], v[178:181], v[92:95]
	v_mfma_f32_16x16x32_bf16 v[84:87], v[146:149], v[186:189], v[84:87]
	v_mfma_f32_16x16x32_bf16 v[76:79], v[154:157], v[186:189], v[76:79]
	v_mfma_f32_16x16x32_bf16 v[124:127], v[150:153], v[166:169], v[124:127]
	v_mfma_f32_16x16x32_bf16 v[120:123], v[158:161], v[166:169], v[120:123]
	v_mfma_f32_16x16x32_bf16 v[116:119], v[150:153], v[174:177], v[116:119]
	v_mfma_f32_16x16x32_bf16 v[108:111], v[158:161], v[174:177], v[108:111]
	v_mfma_f32_16x16x32_bf16 v[100:103], v[150:153], v[182:185], v[100:103]
	v_mfma_f32_16x16x32_bf16 v[92:95], v[158:161], v[182:185], v[92:95]
	v_mfma_f32_16x16x32_bf16 v[84:87], v[150:153], v[190:193], v[84:87]
	v_mfma_f32_16x16x32_bf16 v[76:79], v[158:161], v[190:193], v[76:79]
	v_mfma_f32_16x16x32_bf16 v[112:115], v[130:133], v[162:165], v[112:115]
	v_mfma_f32_16x16x32_bf16 v[104:107], v[138:141], v[162:165], v[104:107]
	v_mfma_f32_16x16x32_bf16 v[96:99], v[130:133], v[170:173], v[96:99]
	v_mfma_f32_16x16x32_bf16 v[88:91], v[138:141], v[170:173], v[88:91]
	v_mfma_f32_16x16x32_bf16 v[80:83], v[130:133], v[178:181], v[80:83]
	v_mfma_f32_16x16x32_bf16 v[72:75], v[138:141], v[178:181], v[72:75]
	v_mfma_f32_16x16x32_bf16 v[68:71], v[130:133], v[186:189], v[68:71]
	v_mfma_f32_16x16x32_bf16 v[64:67], v[138:141], v[186:189], v[64:67]
	v_mfma_f32_16x16x32_bf16 v[112:115], v[134:137], v[166:169], v[112:115]
	v_mfma_f32_16x16x32_bf16 v[104:107], v[142:145], v[166:169], v[104:107]
	v_mfma_f32_16x16x32_bf16 v[96:99], v[134:137], v[174:177], v[96:99]
	v_mfma_f32_16x16x32_bf16 v[88:91], v[142:145], v[174:177], v[88:91]
	v_mfma_f32_16x16x32_bf16 v[80:83], v[134:137], v[182:185], v[80:83]
	v_mfma_f32_16x16x32_bf16 v[72:75], v[142:145], v[182:185], v[72:75]
	v_mfma_f32_16x16x32_bf16 v[68:71], v[134:137], v[190:193], v[68:71]
	v_mfma_f32_16x16x32_bf16 v[64:67], v[142:145], v[190:193], v[64:67]
	s_barrier
	s_add_i32 s24, vcc_lo, s28
	v_lshl_add_u64 v[214:215], v[214:215], 0, s[42:43]
	s_mov_b32 m0, s24
	ds_read_b128 v[186:189], v224 offset:49152
	ds_read_b128 v[190:193], v224 offset:50176
	ds_read_b128 v[178:181], v224 offset:51200
	ds_read_b128 v[182:185], v224 offset:52224
	ds_read_b128 v[170:173], v224 offset:53248
	ds_read_b128 v[174:177], v224 offset:54272
	ds_read_b128 v[162:165], v224 offset:55296
	ds_read_b128 v[166:169], v224 offset:56320
	global_load_lds_dwordx4 v[214:215], off
	s_add_i32 m0, s24, 0x2000
	s_add_u32 s22, s22, 0x80080
	v_lshl_add_u64 v[214:215], v[216:217], 0, s[42:43]
	s_addc_u32 s23, s23, 0
	s_add_i32 s24, vcc_hi, s28
	global_load_lds_dwordx4 v[214:215], off
	v_lshl_add_u64 v[214:215], s[22:23], 0, v[200:201]
	s_mov_b32 m0, s24
	s_and_b64 vcc, exec, s[58:59]
	global_load_lds_dwordx4 v[214:215], off
	v_lshl_add_u64 v[214:215], s[22:23], 0, v[204:205]
	s_add_i32 m0, s24, 0x2000
	s_nop 0
	global_load_lds_dwordx4 v[214:215], off
	v_lshl_add_u64 v[214:215], v[218:219], 0, s[42:43]
	s_mov_b32 m0, s91
	s_nop 0
	global_load_lds_dwordx4 v[214:215], off
	v_lshl_add_u64 v[214:215], v[220:221], 0, s[42:43]
	s_mov_b32 m0, s94
	s_nop 0
	global_load_lds_dwordx4 v[214:215], off
	s_waitcnt vmcnt(8)
	s_waitcnt lgkmcnt(0)
	s_barrier
	s_cbranch_vccnz .LBB0_513
	s_waitcnt lgkmcnt(0)
	v_mfma_f32_16x16x32_bf16 v[60:63], v[146:149], v[186:189], v[60:63]
	v_mfma_f32_16x16x32_bf16 v[56:59], v[154:157], v[186:189], v[56:59]
	v_mfma_f32_16x16x32_bf16 v[44:47], v[146:149], v[178:181], v[44:47]
	v_mfma_f32_16x16x32_bf16 v[40:43], v[154:157], v[178:181], v[40:43]
	v_mfma_f32_16x16x32_bf16 v[28:31], v[146:149], v[170:173], v[28:31]
	v_mfma_f32_16x16x32_bf16 v[24:27], v[154:157], v[170:173], v[24:27]
	v_mfma_f32_16x16x32_bf16 v[12:15], v[146:149], v[162:165], v[12:15]
	v_mfma_f32_16x16x32_bf16 v[8:11], v[154:157], v[162:165], v[8:11]
	v_mfma_f32_16x16x32_bf16 v[60:63], v[150:153], v[190:193], v[60:63]
	v_mfma_f32_16x16x32_bf16 v[56:59], v[158:161], v[190:193], v[56:59]
	v_mfma_f32_16x16x32_bf16 v[44:47], v[150:153], v[182:185], v[44:47]
	v_mfma_f32_16x16x32_bf16 v[40:43], v[158:161], v[182:185], v[40:43]
	v_mfma_f32_16x16x32_bf16 v[28:31], v[150:153], v[174:177], v[28:31]
	v_mfma_f32_16x16x32_bf16 v[24:27], v[158:161], v[174:177], v[24:27]
	v_mfma_f32_16x16x32_bf16 v[12:15], v[150:153], v[166:169], v[12:15]
	v_mfma_f32_16x16x32_bf16 v[8:11], v[158:161], v[166:169], v[8:11]
	v_mfma_f32_16x16x32_bf16 v[52:55], v[130:133], v[186:189], v[52:55]
	v_mfma_f32_16x16x32_bf16 v[48:51], v[138:141], v[186:189], v[48:51]
	v_mfma_f32_16x16x32_bf16 v[36:39], v[130:133], v[178:181], v[36:39]
	v_mfma_f32_16x16x32_bf16 v[32:35], v[138:141], v[178:181], v[32:35]
	v_mfma_f32_16x16x32_bf16 v[20:23], v[130:133], v[170:173], v[20:23]
	v_mfma_f32_16x16x32_bf16 v[16:19], v[138:141], v[170:173], v[16:19]
	v_mfma_f32_16x16x32_bf16 v[4:7], v[130:133], v[162:165], v[4:7]
	v_mfma_f32_16x16x32_bf16 v[0:3], v[138:141], v[162:165], v[0:3]
	v_mfma_f32_16x16x32_bf16 v[52:55], v[134:137], v[190:193], v[52:55]
	v_mfma_f32_16x16x32_bf16 v[48:51], v[142:145], v[190:193], v[48:51]
	v_mfma_f32_16x16x32_bf16 v[36:39], v[134:137], v[182:185], v[36:39]
	v_mfma_f32_16x16x32_bf16 v[32:35], v[142:145], v[182:185], v[32:35]
	v_mfma_f32_16x16x32_bf16 v[20:23], v[134:137], v[174:177], v[20:23]
	v_mfma_f32_16x16x32_bf16 v[16:19], v[142:145], v[174:177], v[16:19]
	v_mfma_f32_16x16x32_bf16 v[4:7], v[134:137], v[166:169], v[4:7]
	v_mfma_f32_16x16x32_bf16 v[0:3], v[142:145], v[166:169], v[0:3]
	s_branch .LBB0_513

.LBB0_725:
	s_add_u32 s2, s64, 0xfffe0080
	s_addc_u32 s3, s65, -1
	s_add_i32 s29, 0, 0x10000
	s_cmp_eq_u32 s66, 4
	s_cselect_b32 s25, s61, s3
	s_cselect_b32 s24, s60, s2
	v_add_u32_e32 v145, s29, v143
	s_cselect_b32 s23, s63, s17
	s_cselect_b32 s22, s62, s15
	s_add_i32 s30, 0, 0x14000
	ds_read_b128 v[146:149], v145
	ds_read_b128 v[150:153], v145 offset:1024
	ds_read_b128 v[154:157], v145 offset:2048
	ds_read_b128 v[158:161], v145 offset:3072
	v_add_u32_e32 v145, s30, v143
	ds_read_b128 v[162:165], v145
	ds_read_b128 v[166:169], v145 offset:1024
	ds_read_b128 v[170:173], v145 offset:2048
	ds_read_b128 v[174:177], v145 offset:3072
	v_lshl_add_u64 v[214:215], s[64:65], 0, v[138:139]
	s_add_i32 m0, s53, 0xc000
	ds_read_b128 v[178:181], v144
	ds_read_b128 v[182:185], v144 offset:1024
	ds_read_b128 v[186:189], v144 offset:2048
	ds_read_b128 v[190:193], v144 offset:3072
	ds_read_b128 v[198:201], v144 offset:4096
	ds_read_b128 v[202:205], v144 offset:5120
	ds_read_b128 v[206:209], v144 offset:6144
	ds_read_b128 v[210:213], v144 offset:7168
	global_load_lds_dwordx4 v[214:215], off
	v_lshl_add_u64 v[214:215], s[64:65], 0, v[140:141]
	s_add_i32 m0, s53, 0xe000
	s_nop 0
	global_load_lds_dwordx4 v[214:215], off
	s_waitcnt vmcnt(8)
	s_waitcnt lgkmcnt(0)
	s_barrier
	v_mfma_f32_16x16x32_bf16 v[124:127], v[146:149], v[178:181], v[124:127]
	v_mfma_f32_16x16x32_bf16 v[120:123], v[154:157], v[178:181], v[120:123]
	v_mfma_f32_16x16x32_bf16 v[116:119], v[146:149], v[186:189], v[116:119]
	v_mfma_f32_16x16x32_bf16 v[108:111], v[154:157], v[186:189], v[108:111]
	v_mfma_f32_16x16x32_bf16 v[100:103], v[146:149], v[198:201], v[100:103]
	v_mfma_f32_16x16x32_bf16 v[92:95], v[154:157], v[198:201], v[92:95]
	v_mfma_f32_16x16x32_bf16 v[84:87], v[146:149], v[206:209], v[84:87]
	v_mfma_f32_16x16x32_bf16 v[76:79], v[154:157], v[206:209], v[76:79]
	v_mfma_f32_16x16x32_bf16 v[124:127], v[150:153], v[182:185], v[124:127]
	v_mfma_f32_16x16x32_bf16 v[120:123], v[158:161], v[182:185], v[120:123]
	v_mfma_f32_16x16x32_bf16 v[116:119], v[150:153], v[190:193], v[116:119]
	v_mfma_f32_16x16x32_bf16 v[108:111], v[158:161], v[190:193], v[108:111]
	v_mfma_f32_16x16x32_bf16 v[100:103], v[150:153], v[202:205], v[100:103]
	v_mfma_f32_16x16x32_bf16 v[92:95], v[158:161], v[202:205], v[92:95]
	v_mfma_f32_16x16x32_bf16 v[84:87], v[150:153], v[210:213], v[84:87]
	v_mfma_f32_16x16x32_bf16 v[76:79], v[158:161], v[210:213], v[76:79]
	v_mfma_f32_16x16x32_bf16 v[112:115], v[162:165], v[178:181], v[112:115]
	v_mfma_f32_16x16x32_bf16 v[104:107], v[170:173], v[178:181], v[104:107]
	v_mfma_f32_16x16x32_bf16 v[96:99], v[162:165], v[186:189], v[96:99]
	v_mfma_f32_16x16x32_bf16 v[88:91], v[170:173], v[186:189], v[88:91]
	v_mfma_f32_16x16x32_bf16 v[80:83], v[162:165], v[198:201], v[80:83]
	v_mfma_f32_16x16x32_bf16 v[72:75], v[170:173], v[198:201], v[72:75]
	v_mfma_f32_16x16x32_bf16 v[68:71], v[162:165], v[206:209], v[68:71]
	v_mfma_f32_16x16x32_bf16 v[64:67], v[170:173], v[206:209], v[64:67]
	v_mfma_f32_16x16x32_bf16 v[112:115], v[166:169], v[182:185], v[112:115]
	v_mfma_f32_16x16x32_bf16 v[104:107], v[174:177], v[182:185], v[104:107]
	v_mfma_f32_16x16x32_bf16 v[96:99], v[166:169], v[190:193], v[96:99]
	v_mfma_f32_16x16x32_bf16 v[88:91], v[174:177], v[190:193], v[88:91]
	v_mfma_f32_16x16x32_bf16 v[80:83], v[166:169], v[202:205], v[80:83]
	v_mfma_f32_16x16x32_bf16 v[72:75], v[174:177], v[202:205], v[72:75]
	v_mfma_f32_16x16x32_bf16 v[68:71], v[166:169], v[210:213], v[68:71]
	v_mfma_f32_16x16x32_bf16 v[64:67], v[174:177], v[210:213], v[64:67]
	s_barrier
	s_add_i32 s2, s29, s39
	v_lshl_add_u64 v[214:215], s[22:23], 0, v[134:135]
	s_mov_b32 m0, s2
	ds_read_b128 v[178:181], v144 offset:16384
	ds_read_b128 v[182:185], v144 offset:17408
	ds_read_b128 v[186:189], v144 offset:18432
	ds_read_b128 v[190:193], v144 offset:19456
	ds_read_b128 v[198:201], v144 offset:20480
	ds_read_b128 v[202:205], v144 offset:21504
	ds_read_b128 v[206:209], v144 offset:22528
	ds_read_b128 v[210:213], v144 offset:23552
	global_load_lds_dwordx4 v[214:215], off
	s_add_i32 m0, s2, 0x2000
	s_add_u32 s2, s22, 0x20000
	v_lshl_add_u64 v[216:217], s[22:23], 0, v[130:131]
	s_addc_u32 s3, s23, 0
	s_add_i32 s29, s30, s39
	global_load_lds_dwordx4 v[216:217], off
	v_lshl_add_u64 v[218:219], s[2:3], 0, v[134:135]
	s_mov_b32 m0, s29
	v_lshl_add_u64 v[220:221], s[24:25], 0, v[132:133]
	global_load_lds_dwordx4 v[218:219], off
	v_lshl_add_u64 v[218:219], s[2:3], 0, v[130:131]
	s_add_i32 m0, s29, 0x2000
	s_nop 0
	global_load_lds_dwordx4 v[218:219], off
	v_lshl_add_u64 v[218:219], s[24:25], 0, v[136:137]
	s_mov_b32 m0, s53
	s_nop 0
	global_load_lds_dwordx4 v[218:219], off
	s_mov_b32 m0, s68
	s_nop 0
	global_load_lds_dwordx4 v[220:221], off
	s_waitcnt vmcnt(8)
	s_waitcnt lgkmcnt(0)
	s_barrier
	v_mfma_f32_16x16x32_bf16 v[60:63], v[146:149], v[178:181], v[60:63]
	v_mfma_f32_16x16x32_bf16 v[56:59], v[154:157], v[178:181], v[56:59]
	v_mfma_f32_16x16x32_bf16 v[52:55], v[146:149], v[186:189], v[52:55]
	v_mfma_f32_16x16x32_bf16 v[44:47], v[154:157], v[186:189], v[44:47]
	v_mfma_f32_16x16x32_bf16 v[36:39], v[146:149], v[198:201], v[36:39]
	v_mfma_f32_16x16x32_bf16 v[28:31], v[154:157], v[198:201], v[28:31]
	v_mfma_f32_16x16x32_bf16 v[20:23], v[146:149], v[206:209], v[20:23]
	v_mfma_f32_16x16x32_bf16 v[12:15], v[154:157], v[206:209], v[12:15]
	v_mfma_f32_16x16x32_bf16 v[60:63], v[150:153], v[182:185], v[60:63]
	v_mfma_f32_16x16x32_bf16 v[56:59], v[158:161], v[182:185], v[56:59]
	v_mfma_f32_16x16x32_bf16 v[52:55], v[150:153], v[190:193], v[52:55]
	v_mfma_f32_16x16x32_bf16 v[44:47], v[158:161], v[190:193], v[44:47]
	v_mfma_f32_16x16x32_bf16 v[36:39], v[150:153], v[202:205], v[36:39]
	v_mfma_f32_16x16x32_bf16 v[28:31], v[158:161], v[202:205], v[28:31]
	v_mfma_f32_16x16x32_bf16 v[20:23], v[150:153], v[210:213], v[20:23]
	v_mfma_f32_16x16x32_bf16 v[12:15], v[158:161], v[210:213], v[12:15]
	v_mfma_f32_16x16x32_bf16 v[48:51], v[162:165], v[178:181], v[48:51]
	v_mfma_f32_16x16x32_bf16 v[40:43], v[170:173], v[178:181], v[40:43]
	v_mfma_f32_16x16x32_bf16 v[32:35], v[162:165], v[186:189], v[32:35]
	v_mfma_f32_16x16x32_bf16 v[24:27], v[170:173], v[186:189], v[24:27]
	v_mfma_f32_16x16x32_bf16 v[16:19], v[162:165], v[198:201], v[16:19]
	v_mfma_f32_16x16x32_bf16 v[8:11], v[170:173], v[198:201], v[8:11]
	v_mfma_f32_16x16x32_bf16 v[4:7], v[162:165], v[206:209], v[4:7]
	v_mfma_f32_16x16x32_bf16 v[0:3], v[170:173], v[206:209], v[0:3]
	v_mfma_f32_16x16x32_bf16 v[48:51], v[166:169], v[182:185], v[48:51]
	v_mfma_f32_16x16x32_bf16 v[40:43], v[174:177], v[182:185], v[40:43]
	v_mfma_f32_16x16x32_bf16 v[32:35], v[166:169], v[190:193], v[32:35]
	v_mfma_f32_16x16x32_bf16 v[24:27], v[174:177], v[190:193], v[24:27]
	v_mfma_f32_16x16x32_bf16 v[16:19], v[166:169], v[202:205], v[16:19]
	v_mfma_f32_16x16x32_bf16 v[8:11], v[174:177], v[202:205], v[8:11]
	v_mfma_f32_16x16x32_bf16 v[4:7], v[166:169], v[210:213], v[4:7]
	v_mfma_f32_16x16x32_bf16 v[0:3], v[174:177], v[210:213], v[0:3]
	s_barrier
	s_add_i32 s29, 0, 0x18000
	v_add_u32_e32 v145, s29, v143
	s_add_i32 s30, 0, 0x1c000
	ds_read_b128 v[146:149], v145
	ds_read_b128 v[150:153], v145 offset:1024
	ds_read_b128 v[154:157], v145 offset:2048
	ds_read_b128 v[158:161], v145 offset:3072
	v_add_u32_e32 v145, s30, v143
	ds_read_b128 v[162:165], v145
	ds_read_b128 v[166:169], v145 offset:1024
	ds_read_b128 v[170:173], v145 offset:2048
	ds_read_b128 v[174:177], v145 offset:3072
	s_add_u32 s2, s24, 0x20000
	s_addc_u32 s3, s25, 0
	s_mov_b32 m0, s69
	v_lshl_add_u64 v[222:223], s[2:3], 0, v[136:137]
	ds_read_b128 v[178:181], v144 offset:32768
	ds_read_b128 v[182:185], v144 offset:33792
	ds_read_b128 v[186:189], v144 offset:34816
	ds_read_b128 v[190:193], v144 offset:35840
	ds_read_b128 v[198:201], v144 offset:36864
	ds_read_b128 v[202:205], v144 offset:37888
	ds_read_b128 v[206:209], v144 offset:38912
	ds_read_b128 v[210:213], v144 offset:39936
	global_load_lds_dwordx4 v[222:223], off
	v_lshl_add_u64 v[222:223], s[2:3], 0, v[132:133]
	s_mov_b32 m0, s70
	s_nop 0
	global_load_lds_dwordx4 v[222:223], off
	s_waitcnt vmcnt(8)
	s_waitcnt lgkmcnt(0)
	s_barrier
	v_mfma_f32_16x16x32_bf16 v[124:127], v[146:149], v[178:181], v[124:127]
	v_mfma_f32_16x16x32_bf16 v[120:123], v[154:157], v[178:181], v[120:123]
	v_mfma_f32_16x16x32_bf16 v[116:119], v[146:149], v[186:189], v[116:119]
	v_mfma_f32_16x16x32_bf16 v[108:111], v[154:157], v[186:189], v[108:111]
	v_mfma_f32_16x16x32_bf16 v[100:103], v[146:149], v[198:201], v[100:103]
	v_mfma_f32_16x16x32_bf16 v[92:95], v[154:157], v[198:201], v[92:95]
	v_mfma_f32_16x16x32_bf16 v[84:87], v[146:149], v[206:209], v[84:87]
	v_mfma_f32_16x16x32_bf16 v[76:79], v[154:157], v[206:209], v[76:79]
	v_mfma_f32_16x16x32_bf16 v[124:127], v[150:153], v[182:185], v[124:127]
	v_mfma_f32_16x16x32_bf16 v[120:123], v[158:161], v[182:185], v[120:123]
	v_mfma_f32_16x16x32_bf16 v[116:119], v[150:153], v[190:193], v[116:119]
	v_mfma_f32_16x16x32_bf16 v[108:111], v[158:161], v[190:193], v[108:111]
	v_mfma_f32_16x16x32_bf16 v[100:103], v[150:153], v[202:205], v[100:103]
	v_mfma_f32_16x16x32_bf16 v[92:95], v[158:161], v[202:205], v[92:95]
	v_mfma_f32_16x16x32_bf16 v[84:87], v[150:153], v[210:213], v[84:87]
	v_mfma_f32_16x16x32_bf16 v[76:79], v[158:161], v[210:213], v[76:79]
	v_mfma_f32_16x16x32_bf16 v[112:115], v[162:165], v[178:181], v[112:115]
	v_mfma_f32_16x16x32_bf16 v[104:107], v[170:173], v[178:181], v[104:107]
	v_mfma_f32_16x16x32_bf16 v[96:99], v[162:165], v[186:189], v[96:99]
	v_mfma_f32_16x16x32_bf16 v[88:91], v[170:173], v[186:189], v[88:91]
	v_mfma_f32_16x16x32_bf16 v[80:83], v[162:165], v[198:201], v[80:83]
	v_mfma_f32_16x16x32_bf16 v[72:75], v[170:173], v[198:201], v[72:75]
	v_mfma_f32_16x16x32_bf16 v[68:71], v[162:165], v[206:209], v[68:71]
	v_mfma_f32_16x16x32_bf16 v[64:67], v[170:173], v[206:209], v[64:67]
	v_mfma_f32_16x16x32_bf16 v[112:115], v[166:169], v[182:185], v[112:115]
	v_mfma_f32_16x16x32_bf16 v[104:107], v[174:177], v[182:185], v[104:107]
	v_mfma_f32_16x16x32_bf16 v[96:99], v[166:169], v[190:193], v[96:99]
	v_mfma_f32_16x16x32_bf16 v[88:91], v[174:177], v[190:193], v[88:91]
	v_mfma_f32_16x16x32_bf16 v[80:83], v[166:169], v[202:205], v[80:83]
	v_mfma_f32_16x16x32_bf16 v[72:75], v[174:177], v[202:205], v[72:75]
	v_mfma_f32_16x16x32_bf16 v[68:71], v[166:169], v[210:213], v[68:71]
	v_mfma_f32_16x16x32_bf16 v[64:67], v[174:177], v[210:213], v[64:67]
	s_barrier
	s_add_i32 s2, s29, s39
	v_lshl_add_u64 v[214:215], v[214:215], 0, s[42:43]
	s_mov_b32 m0, s2
	ds_read_b128 v[178:181], v144 offset:49152
	ds_read_b128 v[182:185], v144 offset:50176
	ds_read_b128 v[186:189], v144 offset:51200
	ds_read_b128 v[190:193], v144 offset:52224
	ds_read_b128 v[198:201], v144 offset:53248
	ds_read_b128 v[202:205], v144 offset:54272
	ds_read_b128 v[206:209], v144 offset:55296
	ds_read_b128 v[210:213], v144 offset:56320
	global_load_lds_dwordx4 v[214:215], off
	s_add_i32 m0, s2, 0x2000
	s_add_u32 s2, s22, 0x20080
	v_lshl_add_u64 v[214:215], v[216:217], 0, s[42:43]
	s_addc_u32 s3, s23, 0
	s_add_i32 s22, s30, s39
	global_load_lds_dwordx4 v[214:215], off
	v_lshl_add_u64 v[214:215], s[2:3], 0, v[134:135]
	s_mov_b32 m0, s22
	s_nop 0
	global_load_lds_dwordx4 v[214:215], off
	v_lshl_add_u64 v[214:215], s[2:3], 0, v[130:131]
	s_add_i32 m0, s22, 0x2000
	s_nop 0
	global_load_lds_dwordx4 v[214:215], off
	v_lshl_add_u64 v[214:215], v[218:219], 0, s[42:43]
	s_mov_b32 m0, s71
	s_nop 0
	global_load_lds_dwordx4 v[214:215], off
	v_lshl_add_u64 v[214:215], v[220:221], 0, s[42:43]
	s_mov_b32 m0, s74
	s_nop 0
	global_load_lds_dwordx4 v[214:215], off
	s_waitcnt vmcnt(8)
	s_waitcnt lgkmcnt(0)
	s_barrier
	v_mfma_f32_16x16x32_bf16 v[60:63], v[146:149], v[178:181], v[60:63]
	v_mfma_f32_16x16x32_bf16 v[56:59], v[154:157], v[178:181], v[56:59]
	v_mfma_f32_16x16x32_bf16 v[52:55], v[146:149], v[186:189], v[52:55]
	v_mfma_f32_16x16x32_bf16 v[44:47], v[154:157], v[186:189], v[44:47]
	v_mfma_f32_16x16x32_bf16 v[36:39], v[146:149], v[198:201], v[36:39]
	v_mfma_f32_16x16x32_bf16 v[28:31], v[154:157], v[198:201], v[28:31]
	v_mfma_f32_16x16x32_bf16 v[20:23], v[146:149], v[206:209], v[20:23]
	v_mfma_f32_16x16x32_bf16 v[12:15], v[154:157], v[206:209], v[12:15]
	v_mfma_f32_16x16x32_bf16 v[60:63], v[150:153], v[182:185], v[60:63]
	v_mfma_f32_16x16x32_bf16 v[56:59], v[158:161], v[182:185], v[56:59]
	v_mfma_f32_16x16x32_bf16 v[52:55], v[150:153], v[190:193], v[52:55]
	v_mfma_f32_16x16x32_bf16 v[44:47], v[158:161], v[190:193], v[44:47]
	v_mfma_f32_16x16x32_bf16 v[36:39], v[150:153], v[202:205], v[36:39]
	v_mfma_f32_16x16x32_bf16 v[28:31], v[158:161], v[202:205], v[28:31]
	v_mfma_f32_16x16x32_bf16 v[20:23], v[150:153], v[210:213], v[20:23]
	v_mfma_f32_16x16x32_bf16 v[12:15], v[158:161], v[210:213], v[12:15]
	v_mfma_f32_16x16x32_bf16 v[48:51], v[162:165], v[178:181], v[48:51]
	v_mfma_f32_16x16x32_bf16 v[40:43], v[170:173], v[178:181], v[40:43]
	v_mfma_f32_16x16x32_bf16 v[32:35], v[162:165], v[186:189], v[32:35]
	v_mfma_f32_16x16x32_bf16 v[24:27], v[170:173], v[186:189], v[24:27]
	v_mfma_f32_16x16x32_bf16 v[16:19], v[162:165], v[198:201], v[16:19]
	v_mfma_f32_16x16x32_bf16 v[8:11], v[170:173], v[198:201], v[8:11]
	v_mfma_f32_16x16x32_bf16 v[4:7], v[162:165], v[206:209], v[4:7]
	v_mfma_f32_16x16x32_bf16 v[0:3], v[170:173], v[206:209], v[0:3]
	v_mfma_f32_16x16x32_bf16 v[48:51], v[166:169], v[182:185], v[48:51]
	v_mfma_f32_16x16x32_bf16 v[40:43], v[174:177], v[182:185], v[40:43]
	v_mfma_f32_16x16x32_bf16 v[32:35], v[166:169], v[190:193], v[32:35]
	v_mfma_f32_16x16x32_bf16 v[24:27], v[174:177], v[190:193], v[24:27]
	v_mfma_f32_16x16x32_bf16 v[16:19], v[166:169], v[202:205], v[16:19]
	v_mfma_f32_16x16x32_bf16 v[8:11], v[174:177], v[202:205], v[8:11]
	v_mfma_f32_16x16x32_bf16 v[4:7], v[166:169], v[210:213], v[4:7]
	v_mfma_f32_16x16x32_bf16 v[0:3], v[174:177], v[210:213], v[0:3]
	s_barrier
	s_add_i32 s66, s66, 2
	s_add_u32 s64, s64, 0x100
	s_addc_u32 s65, s65, 0
	s_add_u32 s15, s15, 0x100
	s_addc_u32 s17, s17, 0
	s_cmp_gt_u32 s66, 5
	s_cbranch_scc0 .LBB0_725
	s_and_b64 vcc, exec, s[10:11]
	s_cbranch_vccz .LBB0_728
	s_barrier

.LBB0_969:
	s_add_u32 s24, s18, s92
	s_addc_u32 s25, s19, s93
	s_add_u32 s60, s24, 0x100
	s_addc_u32 s61, s25, 0
	s_add_u32 s81, s2, s92
	s_addc_u32 s84, s29, s93
	s_add_i32 vcc_lo, 0, 0x10000
	s_cmpk_eq_i32 s92, 0xf00
	s_cselect_b64 s[26:27], -1, 0
	s_and_b64 s[24:25], s[26:27], exec
	s_cselect_b32 s25, s15, s61
	s_cselect_b32 s24, s17, s60
	s_waitcnt lgkmcnt(0)
	v_add_u32_e32 v104, vcc_lo, v234
	s_cselect_b32 s85, s67, s84
	s_cselect_b32 s84, s3, s81
	s_add_i32 s81, 0, 0x14000
	ds_read_b128 v[162:165], v104
	ds_read_b128 v[166:169], v104 offset:1024
	ds_read_b128 v[170:173], v104 offset:2048
	ds_read_b128 v[174:177], v104 offset:3072
	v_add_u32_e32 v104, s81, v234
	ds_read_b128 v[146:149], v104
	ds_read_b128 v[150:153], v104 offset:1024
	ds_read_b128 v[154:157], v104 offset:2048
	ds_read_b128 v[158:161], v104 offset:3072
	v_lshl_add_u64 v[104:105], v[208:209], 0, s[92:93]
	s_add_i32 m0, s53, 0xc000
	ds_read_b128 v[178:181], v236
	ds_read_b128 v[182:185], v236 offset:1024
	ds_read_b128 v[186:189], v236 offset:2048
	ds_read_b128 v[190:193], v236 offset:3072
	ds_read_b128 v[210:213], v236 offset:4096
	ds_read_b128 v[214:217], v236 offset:5120
	ds_read_b128 v[218:221], v236 offset:6144
	ds_read_b128 v[222:225], v236 offset:7168
	global_load_lds_dwordx4 v[104:105], off
	v_lshl_add_u64 v[104:105], v[206:207], 0, s[92:93]
	s_add_i32 m0, s53, 0xe000
	s_nop 0
	global_load_lds_dwordx4 v[104:105], off
	s_waitcnt vmcnt(8)
	s_waitcnt lgkmcnt(0)
	s_barrier
	v_mfma_f32_16x16x32_bf16 v[104:107], v[162:165], v[178:181], v[142:145]
	v_mfma_f32_16x16x32_bf16 v[108:111], v[170:173], v[178:181], v[138:141]
	v_mfma_f32_16x16x32_bf16 v[116:119], v[162:165], v[186:189], v[120:123]
	v_mfma_f32_16x16x32_bf16 v[112:115], v[170:173], v[186:189], v[112:115]
	v_mfma_f32_16x16x32_bf16 v[92:95], v[162:165], v[210:213], v[92:95]
	v_mfma_f32_16x16x32_bf16 v[88:91], v[170:173], v[210:213], v[88:91]
	v_mfma_f32_16x16x32_bf16 v[76:79], v[162:165], v[218:221], v[76:79]
	v_mfma_f32_16x16x32_bf16 v[72:75], v[170:173], v[218:221], v[72:75]
	v_mfma_f32_16x16x32_bf16 v[104:107], v[166:169], v[182:185], v[104:107]
	v_mfma_f32_16x16x32_bf16 v[108:111], v[174:177], v[182:185], v[108:111]
	v_mfma_f32_16x16x32_bf16 v[116:119], v[166:169], v[190:193], v[116:119]
	v_mfma_f32_16x16x32_bf16 v[112:115], v[174:177], v[190:193], v[112:115]
	v_mfma_f32_16x16x32_bf16 v[92:95], v[166:169], v[214:217], v[92:95]
	v_mfma_f32_16x16x32_bf16 v[88:91], v[174:177], v[214:217], v[88:91]
	v_mfma_f32_16x16x32_bf16 v[76:79], v[166:169], v[222:225], v[76:79]
	v_mfma_f32_16x16x32_bf16 v[72:75], v[174:177], v[222:225], v[72:75]
	v_mfma_f32_16x16x32_bf16 v[120:123], v[146:149], v[178:181], v[134:137]
	v_mfma_f32_16x16x32_bf16 v[130:133], v[150:153], v[182:185], v[120:123]
	v_mfma_f32_16x16x32_bf16 v[120:123], v[154:157], v[178:181], v[124:127]
	v_mfma_f32_16x16x32_bf16 v[100:103], v[146:149], v[186:189], v[100:103]
	v_mfma_f32_16x16x32_bf16 v[96:99], v[154:157], v[186:189], v[96:99]
	v_mfma_f32_16x16x32_bf16 v[84:87], v[146:149], v[210:213], v[84:87]
	v_mfma_f32_16x16x32_bf16 v[80:83], v[154:157], v[210:213], v[80:83]
	v_mfma_f32_16x16x32_bf16 v[68:71], v[146:149], v[218:221], v[68:71]
	v_mfma_f32_16x16x32_bf16 v[64:67], v[154:157], v[218:221], v[64:67]
	v_mfma_f32_16x16x32_bf16 v[124:127], v[158:161], v[182:185], v[120:123]
	v_mfma_f32_16x16x32_bf16 v[100:103], v[150:153], v[190:193], v[100:103]
	v_mfma_f32_16x16x32_bf16 v[96:99], v[158:161], v[190:193], v[96:99]
	v_mfma_f32_16x16x32_bf16 v[84:87], v[150:153], v[214:217], v[84:87]
	v_mfma_f32_16x16x32_bf16 v[80:83], v[158:161], v[214:217], v[80:83]
	v_mfma_f32_16x16x32_bf16 v[68:71], v[150:153], v[222:225], v[68:71]
	v_mfma_f32_16x16x32_bf16 v[64:67], v[158:161], v[222:225], v[64:67]
	s_barrier
	s_add_i32 s60, vcc_lo, s39
	v_lshl_add_u64 v[210:211], s[84:85], 0, v[198:199]
	s_mov_b32 m0, s60
	ds_read_b128 v[186:189], v236 offset:16384
	ds_read_b128 v[190:193], v236 offset:17408
	ds_read_b128 v[178:181], v236 offset:18432
	ds_read_b128 v[182:185], v236 offset:19456
	ds_read_b128 v[138:141], v236 offset:20480
	ds_read_b128 v[142:145], v236 offset:21504
	ds_read_b128 v[120:123], v236 offset:22528
	ds_read_b128 v[134:137], v236 offset:23552
	global_load_lds_dwordx4 v[210:211], off
	s_add_i32 m0, s60, 0x2000
	s_add_u32 s60, s84, 0x80000
	v_lshl_add_u64 v[212:213], s[84:85], 0, v[200:201]
	s_addc_u32 s61, s85, 0
	s_add_i32 s81, s81, s39
	global_load_lds_dwordx4 v[212:213], off
	v_lshl_add_u64 v[214:215], s[60:61], 0, v[198:199]
	s_mov_b32 m0, s81
	v_lshl_add_u64 v[216:217], s[24:25], 0, v[200:201]
	global_load_lds_dwordx4 v[214:215], off
	v_lshl_add_u64 v[214:215], s[60:61], 0, v[200:201]
	s_add_i32 m0, s81, 0x2000
	v_cndmask_b32_e64 v128, 0, 1, s[96:97]
	global_load_lds_dwordx4 v[214:215], off
	v_lshl_add_u64 v[214:215], s[24:25], 0, v[198:199]
	s_mov_b32 m0, s53
	v_cmp_ne_u32_e64 s[60:61], 1, v128
	global_load_lds_dwordx4 v[214:215], off
	s_mov_b32 m0, s88
	s_andn2_b64 vcc, exec, s[96:97]
	global_load_lds_dwordx4 v[216:217], off
	s_waitcnt vmcnt(8)
	s_waitcnt lgkmcnt(0)
	s_barrier
	s_cbranch_vccnz .LBB0_971
	s_waitcnt lgkmcnt(0)
	v_mfma_f32_16x16x32_bf16 v[60:63], v[162:165], v[186:189], v[60:63]
	v_mfma_f32_16x16x32_bf16 v[56:59], v[170:173], v[186:189], v[56:59]
	v_mfma_f32_16x16x32_bf16 v[44:47], v[162:165], v[178:181], v[44:47]
	v_mfma_f32_16x16x32_bf16 v[40:43], v[170:173], v[178:181], v[40:43]
	v_mfma_f32_16x16x32_bf16 v[28:31], v[162:165], v[138:141], v[28:31]
	v_mfma_f32_16x16x32_bf16 v[24:27], v[170:173], v[138:141], v[24:27]
	v_mfma_f32_16x16x32_bf16 v[12:15], v[162:165], v[120:123], v[12:15]
	v_mfma_f32_16x16x32_bf16 v[8:11], v[170:173], v[120:123], v[8:11]
	v_mfma_f32_16x16x32_bf16 v[60:63], v[166:169], v[190:193], v[60:63]
	v_mfma_f32_16x16x32_bf16 v[56:59], v[174:177], v[190:193], v[56:59]
	v_mfma_f32_16x16x32_bf16 v[44:47], v[166:169], v[182:185], v[44:47]
	v_mfma_f32_16x16x32_bf16 v[40:43], v[174:177], v[182:185], v[40:43]
	v_mfma_f32_16x16x32_bf16 v[28:31], v[166:169], v[142:145], v[28:31]
	v_mfma_f32_16x16x32_bf16 v[24:27], v[174:177], v[142:145], v[24:27]
	v_mfma_f32_16x16x32_bf16 v[12:15], v[166:169], v[134:137], v[12:15]
	v_mfma_f32_16x16x32_bf16 v[8:11], v[174:177], v[134:137], v[8:11]
	v_mfma_f32_16x16x32_bf16 v[52:55], v[146:149], v[186:189], v[52:55]
	v_mfma_f32_16x16x32_bf16 v[48:51], v[154:157], v[186:189], v[48:51]
	v_mfma_f32_16x16x32_bf16 v[36:39], v[146:149], v[178:181], v[36:39]
	v_mfma_f32_16x16x32_bf16 v[32:35], v[154:157], v[178:181], v[32:35]
	v_mfma_f32_16x16x32_bf16 v[20:23], v[146:149], v[138:141], v[20:23]
	v_mfma_f32_16x16x32_bf16 v[16:19], v[154:157], v[138:141], v[16:19]
	v_mfma_f32_16x16x32_bf16 v[4:7], v[146:149], v[120:123], v[4:7]
	v_mfma_f32_16x16x32_bf16 v[0:3], v[154:157], v[120:123], v[0:3]
	v_mfma_f32_16x16x32_bf16 v[52:55], v[150:153], v[190:193], v[52:55]
	v_mfma_f32_16x16x32_bf16 v[48:51], v[158:161], v[190:193], v[48:51]
	v_mfma_f32_16x16x32_bf16 v[36:39], v[150:153], v[182:185], v[36:39]
	v_mfma_f32_16x16x32_bf16 v[32:35], v[158:161], v[182:185], v[32:35]
	v_mfma_f32_16x16x32_bf16 v[20:23], v[150:153], v[142:145], v[20:23]
	v_mfma_f32_16x16x32_bf16 v[16:19], v[158:161], v[142:145], v[16:19]
	v_mfma_f32_16x16x32_bf16 v[4:7], v[150:153], v[134:137], v[4:7]
	v_mfma_f32_16x16x32_bf16 v[0:3], v[158:161], v[134:137], v[0:3]
.LBB0_971:
	s_barrier
	s_add_i32 s81, 0, 0x18000
	s_waitcnt lgkmcnt(0)
	v_add_u32_e32 v120, s81, v234
	s_add_i32 vcc_lo, 0, 0x1c000
	ds_read_b128 v[162:165], v120
	ds_read_b128 v[166:169], v120 offset:1024
	ds_read_b128 v[170:173], v120 offset:2048
	ds_read_b128 v[174:177], v120 offset:3072
	v_add_u32_e32 v120, vcc_lo, v234
	ds_read_b128 v[146:149], v120
	ds_read_b128 v[150:153], v120 offset:1024
	ds_read_b128 v[154:157], v120 offset:2048
	ds_read_b128 v[158:161], v120 offset:3072
	s_and_b64 s[26:27], s[26:27], exec
	s_cselect_b32 s27, s72, s20
	s_cselect_b32 s26, 0, s21
	s_add_u32 s24, s24, s27
	s_addc_u32 s25, s25, s26
	s_mov_b32 m0, s89
	v_lshl_add_u64 v[120:121], s[24:25], 0, v[198:199]
	ds_read_b128 v[178:181], v236 offset:32768
	ds_read_b128 v[182:185], v236 offset:33792
	ds_read_b128 v[186:189], v236 offset:34816
	ds_read_b128 v[190:193], v236 offset:35840
	ds_read_b128 v[218:221], v236 offset:36864
	ds_read_b128 v[222:225], v236 offset:37888
	ds_read_b128 v[226:229], v236 offset:38912
	ds_read_b128 v[238:241], v236 offset:39936
	global_load_lds_dwordx4 v[120:121], off
	v_lshl_add_u64 v[120:121], s[24:25], 0, v[200:201]
	s_mov_b32 m0, s90
	s_nop 0
	global_load_lds_dwordx4 v[120:121], off
	s_waitcnt vmcnt(8)
	s_waitcnt lgkmcnt(0)
	s_barrier
	v_mfma_f32_16x16x32_bf16 v[104:107], v[162:165], v[178:181], v[104:107]
	v_mfma_f32_16x16x32_bf16 v[142:145], v[166:169], v[182:185], v[104:107]
	v_mfma_f32_16x16x32_bf16 v[104:107], v[170:173], v[178:181], v[108:111]
	v_mfma_f32_16x16x32_bf16 v[138:141], v[174:177], v[182:185], v[104:107]
	v_mfma_f32_16x16x32_bf16 v[104:107], v[162:165], v[186:189], v[116:119]
	v_mfma_f32_16x16x32_bf16 v[120:123], v[166:169], v[190:193], v[104:107]
	v_mfma_f32_16x16x32_bf16 v[104:107], v[170:173], v[186:189], v[112:115]
	v_mfma_f32_16x16x32_bf16 v[92:95], v[162:165], v[218:221], v[92:95]
	v_mfma_f32_16x16x32_bf16 v[88:91], v[170:173], v[218:221], v[88:91]
	v_mfma_f32_16x16x32_bf16 v[76:79], v[162:165], v[226:229], v[76:79]
	v_mfma_f32_16x16x32_bf16 v[72:75], v[170:173], v[226:229], v[72:75]
	v_mfma_f32_16x16x32_bf16 v[112:115], v[174:177], v[190:193], v[104:107]
	v_mfma_f32_16x16x32_bf16 v[92:95], v[166:169], v[222:225], v[92:95]
	v_mfma_f32_16x16x32_bf16 v[88:91], v[174:177], v[222:225], v[88:91]
	v_mfma_f32_16x16x32_bf16 v[76:79], v[166:169], v[238:241], v[76:79]
	v_mfma_f32_16x16x32_bf16 v[72:75], v[174:177], v[238:241], v[72:75]
	v_mfma_f32_16x16x32_bf16 v[104:107], v[146:149], v[178:181], v[130:133]
	v_mfma_f32_16x16x32_bf16 v[134:137], v[150:153], v[182:185], v[104:107]
	v_mfma_f32_16x16x32_bf16 v[104:107], v[154:157], v[178:181], v[124:127]
	v_mfma_f32_16x16x32_bf16 v[100:103], v[146:149], v[186:189], v[100:103]
	v_mfma_f32_16x16x32_bf16 v[96:99], v[154:157], v[186:189], v[96:99]
	v_mfma_f32_16x16x32_bf16 v[84:87], v[146:149], v[218:221], v[84:87]
	v_mfma_f32_16x16x32_bf16 v[80:83], v[154:157], v[218:221], v[80:83]
	v_mfma_f32_16x16x32_bf16 v[68:71], v[146:149], v[226:229], v[68:71]
	v_mfma_f32_16x16x32_bf16 v[64:67], v[154:157], v[226:229], v[64:67]
	v_mfma_f32_16x16x32_bf16 v[124:127], v[158:161], v[182:185], v[104:107]
	v_mfma_f32_16x16x32_bf16 v[100:103], v[150:153], v[190:193], v[100:103]
	v_mfma_f32_16x16x32_bf16 v[96:99], v[158:161], v[190:193], v[96:99]
	v_mfma_f32_16x16x32_bf16 v[84:87], v[150:153], v[222:225], v[84:87]
	v_mfma_f32_16x16x32_bf16 v[80:83], v[158:161], v[222:225], v[80:83]
	v_mfma_f32_16x16x32_bf16 v[68:71], v[150:153], v[238:241], v[68:71]
	v_mfma_f32_16x16x32_bf16 v[64:67], v[158:161], v[238:241], v[64:67]
	s_barrier
	s_add_i32 s24, s81, s39
	v_lshl_add_u64 v[210:211], v[210:211], 0, s[42:43]
	s_mov_b32 m0, s24
	ds_read_b128 v[186:189], v236 offset:49152
	ds_read_b128 v[190:193], v236 offset:50176
	ds_read_b128 v[178:181], v236 offset:51200
	ds_read_b128 v[182:185], v236 offset:52224
	ds_read_b128 v[116:119], v236 offset:53248
	ds_read_b128 v[130:133], v236 offset:54272
	ds_read_b128 v[104:107], v236 offset:55296
	ds_read_b128 v[108:111], v236 offset:56320
	global_load_lds_dwordx4 v[210:211], off
	s_add_i32 m0, s24, 0x2000
	s_add_u32 s24, s84, 0x80080
	v_lshl_add_u64 v[210:211], v[212:213], 0, s[42:43]
	s_addc_u32 s25, s85, 0
	s_add_i32 s26, vcc_lo, s39
	global_load_lds_dwordx4 v[210:211], off
	v_lshl_add_u64 v[210:211], s[24:25], 0, v[198:199]
	s_mov_b32 m0, s26
	s_and_b64 vcc, exec, s[60:61]
	global_load_lds_dwordx4 v[210:211], off
	v_lshl_add_u64 v[210:211], s[24:25], 0, v[200:201]
	s_add_i32 m0, s26, 0x2000
	s_nop 0
	global_load_lds_dwordx4 v[210:211], off
	v_lshl_add_u64 v[210:211], v[214:215], 0, s[42:43]
	s_mov_b32 m0, s94
	s_nop 0
	global_load_lds_dwordx4 v[210:211], off
	v_lshl_add_u64 v[210:211], v[216:217], 0, s[42:43]
	s_mov_b32 m0, s33
	s_nop 0
	global_load_lds_dwordx4 v[210:211], off
	s_waitcnt vmcnt(8)
	s_waitcnt lgkmcnt(0)
	s_barrier
	s_cbranch_vccnz .LBB0_968
	s_waitcnt lgkmcnt(0)
	v_mfma_f32_16x16x32_bf16 v[60:63], v[162:165], v[186:189], v[60:63]
	v_mfma_f32_16x16x32_bf16 v[56:59], v[170:173], v[186:189], v[56:59]
	v_mfma_f32_16x16x32_bf16 v[44:47], v[162:165], v[178:181], v[44:47]
	v_mfma_f32_16x16x32_bf16 v[40:43], v[170:173], v[178:181], v[40:43]
	v_mfma_f32_16x16x32_bf16 v[28:31], v[162:165], v[116:119], v[28:31]
	v_mfma_f32_16x16x32_bf16 v[24:27], v[170:173], v[116:119], v[24:27]
	v_mfma_f32_16x16x32_bf16 v[12:15], v[162:165], v[104:107], v[12:15]
	v_mfma_f32_16x16x32_bf16 v[8:11], v[170:173], v[104:107], v[8:11]
	v_mfma_f32_16x16x32_bf16 v[60:63], v[166:169], v[190:193], v[60:63]
	v_mfma_f32_16x16x32_bf16 v[56:59], v[174:177], v[190:193], v[56:59]
	v_mfma_f32_16x16x32_bf16 v[44:47], v[166:169], v[182:185], v[44:47]
	v_mfma_f32_16x16x32_bf16 v[40:43], v[174:177], v[182:185], v[40:43]
	v_mfma_f32_16x16x32_bf16 v[28:31], v[166:169], v[130:133], v[28:31]
	v_mfma_f32_16x16x32_bf16 v[24:27], v[174:177], v[130:133], v[24:27]
	v_mfma_f32_16x16x32_bf16 v[12:15], v[166:169], v[108:111], v[12:15]
	v_mfma_f32_16x16x32_bf16 v[8:11], v[174:177], v[108:111], v[8:11]
	v_mfma_f32_16x16x32_bf16 v[52:55], v[146:149], v[186:189], v[52:55]
	v_mfma_f32_16x16x32_bf16 v[48:51], v[154:157], v[186:189], v[48:51]
	v_mfma_f32_16x16x32_bf16 v[36:39], v[146:149], v[178:181], v[36:39]
	v_mfma_f32_16x16x32_bf16 v[32:35], v[154:157], v[178:181], v[32:35]
	v_mfma_f32_16x16x32_bf16 v[20:23], v[146:149], v[116:119], v[20:23]
	v_mfma_f32_16x16x32_bf16 v[16:19], v[154:157], v[116:119], v[16:19]
	v_mfma_f32_16x16x32_bf16 v[4:7], v[146:149], v[104:107], v[4:7]
	v_mfma_f32_16x16x32_bf16 v[0:3], v[154:157], v[104:107], v[0:3]
	v_mfma_f32_16x16x32_bf16 v[52:55], v[150:153], v[190:193], v[52:55]
	v_mfma_f32_16x16x32_bf16 v[48:51], v[158:161], v[190:193], v[48:51]
	v_mfma_f32_16x16x32_bf16 v[36:39], v[150:153], v[182:185], v[36:39]
	v_mfma_f32_16x16x32_bf16 v[32:35], v[158:161], v[182:185], v[32:35]
	v_mfma_f32_16x16x32_bf16 v[20:23], v[150:153], v[130:133], v[20:23]
	v_mfma_f32_16x16x32_bf16 v[16:19], v[158:161], v[130:133], v[16:19]
	v_mfma_f32_16x16x32_bf16 v[4:7], v[150:153], v[108:111], v[4:7]
	v_mfma_f32_16x16x32_bf16 v[0:3], v[158:161], v[108:111], v[0:3]
	s_branch .LBB0_968

.LBB0_1400:
	s_add_u32 s2, s64, s74
	s_addc_u32 s3, s65, s75
	s_add_u32 s22, s2, 0x28c00100
	s_addc_u32 s23, s3, 0
	s_cmpk_eq_i32 s74, 0xf00
	s_cselect_b64 s[60:61], -1, 0
	s_and_b64 s[2:3], s[60:61], exec
	s_cselect_b32 s23, s9, s23
	s_cselect_b32 s22, s8, s22
	v_add_u32_e32 v128, s26, v242
	s_add_i32 s2, 0, 0x14000
	v_lshl_add_u64 v[146:147], v[220:221], 0, s[74:75]
	ds_read_b128 v[130:133], v128
	ds_read_b128 v[134:137], v128 offset:1024
	ds_read_b128 v[138:141], v128 offset:2048
	ds_read_b128 v[142:145], v128 offset:3072
	v_add_u32_e32 v128, s2, v242
	v_cndmask_b32_e64 v223, v147, v207, s[60:61]
	v_cndmask_b32_e64 v222, v146, v206, s[60:61]
	ds_read_b128 v[146:149], v128
	ds_read_b128 v[150:153], v128 offset:1024
	ds_read_b128 v[154:157], v128 offset:2048
	ds_read_b128 v[158:161], v128 offset:3072
	v_lshl_add_u64 v[194:195], v[218:219], 0, s[74:75]
	s_add_i32 m0, s36, 0xc000
	s_waitcnt lgkmcnt(0)
	ds_read_b128 v[162:165], v209
	ds_read_b128 v[166:169], v209 offset:1024
	ds_read_b128 v[170:173], v209 offset:2048
	ds_read_b128 v[174:177], v209 offset:3072
	ds_read_b128 v[178:181], v209 offset:4096
	ds_read_b128 v[182:185], v209 offset:5120
	ds_read_b128 v[186:189], v209 offset:6144
	ds_read_b128 v[190:193], v209 offset:7168
	global_load_lds_dwordx4 v[194:195], off
	v_lshl_add_u64 v[194:195], v[216:217], 0, s[74:75]
	s_add_i32 m0, s36, 0xe000
	s_nop 0
	global_load_lds_dwordx4 v[194:195], off
	s_waitcnt vmcnt(8)
	s_waitcnt lgkmcnt(0)
	s_barrier
	v_mfma_f32_16x16x32_bf16 v[124:127], v[130:133], v[162:165], v[124:127]
	v_mfma_f32_16x16x32_bf16 v[120:123], v[138:141], v[162:165], v[120:123]
	v_mfma_f32_16x16x32_bf16 v[108:111], v[130:133], v[170:173], v[108:111]
	v_mfma_f32_16x16x32_bf16 v[104:107], v[138:141], v[170:173], v[104:107]
	v_mfma_f32_16x16x32_bf16 v[92:95], v[130:133], v[178:181], v[92:95]
	v_mfma_f32_16x16x32_bf16 v[88:91], v[138:141], v[178:181], v[88:91]
	v_mfma_f32_16x16x32_bf16 v[76:79], v[130:133], v[186:189], v[76:79]
	v_mfma_f32_16x16x32_bf16 v[72:75], v[138:141], v[186:189], v[72:75]
	v_mfma_f32_16x16x32_bf16 v[124:127], v[134:137], v[166:169], v[124:127]
	v_mfma_f32_16x16x32_bf16 v[120:123], v[142:145], v[166:169], v[120:123]
	v_mfma_f32_16x16x32_bf16 v[108:111], v[134:137], v[174:177], v[108:111]
	v_mfma_f32_16x16x32_bf16 v[104:107], v[142:145], v[174:177], v[104:107]
	v_mfma_f32_16x16x32_bf16 v[92:95], v[134:137], v[182:185], v[92:95]
	v_mfma_f32_16x16x32_bf16 v[88:91], v[142:145], v[182:185], v[88:91]
	v_mfma_f32_16x16x32_bf16 v[76:79], v[134:137], v[190:193], v[76:79]
	v_mfma_f32_16x16x32_bf16 v[72:75], v[142:145], v[190:193], v[72:75]
	v_mfma_f32_16x16x32_bf16 v[116:119], v[146:149], v[162:165], v[116:119]
	v_mfma_f32_16x16x32_bf16 v[112:115], v[154:157], v[162:165], v[112:115]
	v_mfma_f32_16x16x32_bf16 v[100:103], v[146:149], v[170:173], v[100:103]
	v_mfma_f32_16x16x32_bf16 v[96:99], v[154:157], v[170:173], v[96:99]
	v_mfma_f32_16x16x32_bf16 v[84:87], v[146:149], v[178:181], v[84:87]
	v_mfma_f32_16x16x32_bf16 v[80:83], v[154:157], v[178:181], v[80:83]
	v_mfma_f32_16x16x32_bf16 v[68:71], v[146:149], v[186:189], v[68:71]
	v_mfma_f32_16x16x32_bf16 v[64:67], v[154:157], v[186:189], v[64:67]
	v_mfma_f32_16x16x32_bf16 v[116:119], v[150:153], v[166:169], v[116:119]
	v_mfma_f32_16x16x32_bf16 v[112:115], v[158:161], v[166:169], v[112:115]
	v_mfma_f32_16x16x32_bf16 v[100:103], v[150:153], v[174:177], v[100:103]
	v_mfma_f32_16x16x32_bf16 v[96:99], v[158:161], v[174:177], v[96:99]
	v_mfma_f32_16x16x32_bf16 v[84:87], v[150:153], v[182:185], v[84:87]
	v_mfma_f32_16x16x32_bf16 v[80:83], v[158:161], v[182:185], v[80:83]
	v_mfma_f32_16x16x32_bf16 v[68:71], v[150:153], v[190:193], v[68:71]
	v_mfma_f32_16x16x32_bf16 v[64:67], v[158:161], v[190:193], v[64:67]
	s_barrier
	s_add_i32 s3, s26, s33
	v_lshl_add_u64 v[224:225], v[222:223], 0, v[198:199]
	s_mov_b32 m0, s3
	ds_read_b128 v[186:189], v209 offset:16384
	ds_read_b128 v[190:193], v209 offset:17408
	ds_read_b128 v[178:181], v209 offset:18432
	ds_read_b128 v[182:185], v209 offset:19456
	ds_read_b128 v[170:173], v209 offset:20480
	ds_read_b128 v[174:177], v209 offset:21504
	ds_read_b128 v[162:165], v209 offset:22528
	ds_read_b128 v[166:169], v209 offset:23552
	global_load_lds_dwordx4 v[224:225], off
	v_lshl_add_u64 v[226:227], v[222:223], 0, v[200:201]
	s_add_i32 m0, s3, 0x2000
	v_lshl_add_u64 v[194:195], v[222:223], 0, s[40:41]
	s_add_i32 s2, s2, s33
	global_load_lds_dwordx4 v[226:227], off
	v_lshl_add_u64 v[196:197], v[194:195], 0, v[198:199]
	s_mov_b32 m0, s2
	v_lshl_add_u64 v[194:195], v[194:195], 0, v[200:201]
	global_load_lds_dwordx4 v[196:197], off
	s_add_i32 m0, s2, 0x2000
	v_cndmask_b32_e64 v128, v208, v211, s[60:61]
	global_load_lds_dwordx4 v[194:195], off
	s_mov_b32 m0, s36
	v_cndmask_b32_e64 v228, v210, v243, s[60:61]
	global_load_lds_dwordx4 v128, s[22:23]
	s_mov_b32 m0, s37
	v_cndmask_b32_e64 v194, 0, 1, s[20:21]
	global_load_lds_dwordx4 v228, s[22:23]
	s_waitcnt vmcnt(8)
	s_waitcnt lgkmcnt(0)
	v_cmp_ne_u32_e64 s[62:63], 1, v194
	s_andn2_b64 vcc, exec, s[20:21]
	s_barrier
	s_cbranch_vccnz .LBB0_1402
	s_waitcnt lgkmcnt(0)
	v_mfma_f32_16x16x32_bf16 v[60:63], v[130:133], v[186:189], v[60:63]
	v_mfma_f32_16x16x32_bf16 v[56:59], v[138:141], v[186:189], v[56:59]
	v_mfma_f32_16x16x32_bf16 v[44:47], v[130:133], v[178:181], v[44:47]
	v_mfma_f32_16x16x32_bf16 v[40:43], v[138:141], v[178:181], v[40:43]
	v_mfma_f32_16x16x32_bf16 v[28:31], v[130:133], v[170:173], v[28:31]
	v_mfma_f32_16x16x32_bf16 v[24:27], v[138:141], v[170:173], v[24:27]
	v_mfma_f32_16x16x32_bf16 v[12:15], v[130:133], v[162:165], v[12:15]
	v_mfma_f32_16x16x32_bf16 v[8:11], v[138:141], v[162:165], v[8:11]
	v_mfma_f32_16x16x32_bf16 v[60:63], v[134:137], v[190:193], v[60:63]
	v_mfma_f32_16x16x32_bf16 v[56:59], v[142:145], v[190:193], v[56:59]
	v_mfma_f32_16x16x32_bf16 v[44:47], v[134:137], v[182:185], v[44:47]
	v_mfma_f32_16x16x32_bf16 v[40:43], v[142:145], v[182:185], v[40:43]
	v_mfma_f32_16x16x32_bf16 v[28:31], v[134:137], v[174:177], v[28:31]
	v_mfma_f32_16x16x32_bf16 v[24:27], v[142:145], v[174:177], v[24:27]
	v_mfma_f32_16x16x32_bf16 v[12:15], v[134:137], v[166:169], v[12:15]
	v_mfma_f32_16x16x32_bf16 v[8:11], v[142:145], v[166:169], v[8:11]
	v_mfma_f32_16x16x32_bf16 v[52:55], v[146:149], v[186:189], v[52:55]
	v_mfma_f32_16x16x32_bf16 v[48:51], v[154:157], v[186:189], v[48:51]
	v_mfma_f32_16x16x32_bf16 v[36:39], v[146:149], v[178:181], v[36:39]
	v_mfma_f32_16x16x32_bf16 v[32:35], v[154:157], v[178:181], v[32:35]
	v_mfma_f32_16x16x32_bf16 v[20:23], v[146:149], v[170:173], v[20:23]
	v_mfma_f32_16x16x32_bf16 v[16:19], v[154:157], v[170:173], v[16:19]
	v_mfma_f32_16x16x32_bf16 v[4:7], v[146:149], v[162:165], v[4:7]
	v_mfma_f32_16x16x32_bf16 v[0:3], v[154:157], v[162:165], v[0:3]
	v_mfma_f32_16x16x32_bf16 v[52:55], v[150:153], v[190:193], v[52:55]
	v_mfma_f32_16x16x32_bf16 v[48:51], v[158:161], v[190:193], v[48:51]
	v_mfma_f32_16x16x32_bf16 v[36:39], v[150:153], v[182:185], v[36:39]
	v_mfma_f32_16x16x32_bf16 v[32:35], v[158:161], v[182:185], v[32:35]
	v_mfma_f32_16x16x32_bf16 v[20:23], v[150:153], v[174:177], v[20:23]
	v_mfma_f32_16x16x32_bf16 v[16:19], v[158:161], v[174:177], v[16:19]
	v_mfma_f32_16x16x32_bf16 v[4:7], v[150:153], v[166:169], v[4:7]
	v_mfma_f32_16x16x32_bf16 v[0:3], v[158:161], v[166:169], v[0:3]
.LBB0_1402:
	v_mov_b32_e32 v229, v129
	v_lshl_add_u64 v[194:195], s[22:23], 0, v[128:129]
	v_lshl_add_u64 v[196:197], s[22:23], 0, v[228:229]
	s_barrier
	s_add_i32 s2, 0, 0x18000
	v_add_u32_e32 v128, s2, v242
	s_add_i32 s3, 0, 0x1c000
	ds_read_b128 v[146:149], v128
	ds_read_b128 v[150:153], v128 offset:1024
	ds_read_b128 v[154:157], v128 offset:2048
	ds_read_b128 v[158:161], v128 offset:3072
	v_add_u32_e32 v128, s3, v242
	ds_read_b128 v[130:133], v128
	ds_read_b128 v[134:137], v128 offset:1024
	ds_read_b128 v[138:141], v128 offset:2048
	ds_read_b128 v[142:145], v128 offset:3072
	s_mov_b32 m0, s38
	v_cndmask_b32_e64 v128, v212, v244, s[60:61]
	s_waitcnt lgkmcnt(0)
	ds_read_b128 v[162:165], v209 offset:32768
	ds_read_b128 v[166:169], v209 offset:33792
	ds_read_b128 v[170:173], v209 offset:34816
	ds_read_b128 v[174:177], v209 offset:35840
	ds_read_b128 v[178:181], v209 offset:36864
	ds_read_b128 v[182:185], v209 offset:37888
	ds_read_b128 v[186:189], v209 offset:38912
	ds_read_b128 v[190:193], v209 offset:39936
	global_load_lds_dwordx4 v128, s[22:23]
	v_cndmask_b32_e64 v128, v214, v245, s[60:61]
	s_mov_b32 m0, s39
	s_nop 0
	global_load_lds_dwordx4 v128, s[22:23]
	s_waitcnt vmcnt(8)
	s_waitcnt lgkmcnt(0)
	s_barrier
	v_mfma_f32_16x16x32_bf16 v[124:127], v[146:149], v[162:165], v[124:127]
	v_mfma_f32_16x16x32_bf16 v[120:123], v[154:157], v[162:165], v[120:123]
	v_mfma_f32_16x16x32_bf16 v[108:111], v[146:149], v[170:173], v[108:111]
	v_mfma_f32_16x16x32_bf16 v[104:107], v[154:157], v[170:173], v[104:107]
	v_mfma_f32_16x16x32_bf16 v[92:95], v[146:149], v[178:181], v[92:95]
	v_mfma_f32_16x16x32_bf16 v[88:91], v[154:157], v[178:181], v[88:91]
	v_mfma_f32_16x16x32_bf16 v[76:79], v[146:149], v[186:189], v[76:79]
	v_mfma_f32_16x16x32_bf16 v[72:75], v[154:157], v[186:189], v[72:75]
	v_mfma_f32_16x16x32_bf16 v[124:127], v[150:153], v[166:169], v[124:127]
	v_mfma_f32_16x16x32_bf16 v[120:123], v[158:161], v[166:169], v[120:123]
	v_mfma_f32_16x16x32_bf16 v[108:111], v[150:153], v[174:177], v[108:111]
	v_mfma_f32_16x16x32_bf16 v[104:107], v[158:161], v[174:177], v[104:107]
	v_mfma_f32_16x16x32_bf16 v[92:95], v[150:153], v[182:185], v[92:95]
	v_mfma_f32_16x16x32_bf16 v[88:91], v[158:161], v[182:185], v[88:91]
	v_mfma_f32_16x16x32_bf16 v[76:79], v[150:153], v[190:193], v[76:79]
	v_mfma_f32_16x16x32_bf16 v[72:75], v[158:161], v[190:193], v[72:75]
	v_mfma_f32_16x16x32_bf16 v[116:119], v[130:133], v[162:165], v[116:119]
	v_mfma_f32_16x16x32_bf16 v[112:115], v[138:141], v[162:165], v[112:115]
	v_mfma_f32_16x16x32_bf16 v[100:103], v[130:133], v[170:173], v[100:103]
	v_mfma_f32_16x16x32_bf16 v[96:99], v[138:141], v[170:173], v[96:99]
	v_mfma_f32_16x16x32_bf16 v[84:87], v[130:133], v[178:181], v[84:87]
	v_mfma_f32_16x16x32_bf16 v[80:83], v[138:141], v[178:181], v[80:83]
	v_mfma_f32_16x16x32_bf16 v[68:71], v[130:133], v[186:189], v[68:71]
	v_mfma_f32_16x16x32_bf16 v[64:67], v[138:141], v[186:189], v[64:67]
	v_mfma_f32_16x16x32_bf16 v[116:119], v[134:137], v[166:169], v[116:119]
	v_mfma_f32_16x16x32_bf16 v[112:115], v[142:145], v[166:169], v[112:115]
	v_mfma_f32_16x16x32_bf16 v[100:103], v[134:137], v[174:177], v[100:103]
	v_mfma_f32_16x16x32_bf16 v[96:99], v[142:145], v[174:177], v[96:99]
	v_mfma_f32_16x16x32_bf16 v[84:87], v[134:137], v[182:185], v[84:87]
	v_mfma_f32_16x16x32_bf16 v[80:83], v[142:145], v[182:185], v[80:83]
	v_mfma_f32_16x16x32_bf16 v[68:71], v[134:137], v[190:193], v[68:71]
	v_mfma_f32_16x16x32_bf16 v[64:67], v[142:145], v[190:193], v[64:67]
	s_barrier
	s_add_i32 s2, s2, s33
	v_lshl_add_u64 v[224:225], v[224:225], 0, s[42:43]
	s_mov_b32 m0, s2
	ds_read_b128 v[186:189], v209 offset:49152
	ds_read_b128 v[190:193], v209 offset:50176
	ds_read_b128 v[178:181], v209 offset:51200
	ds_read_b128 v[182:185], v209 offset:52224
	ds_read_b128 v[170:173], v209 offset:53248
	ds_read_b128 v[174:177], v209 offset:54272
	ds_read_b128 v[162:165], v209 offset:55296
	ds_read_b128 v[166:169], v209 offset:56320
	global_load_lds_dwordx4 v[224:225], off
	v_lshl_add_u64 v[224:225], v[226:227], 0, s[42:43]
	s_add_i32 m0, s2, 0x2000
	v_lshl_add_u64 v[222:223], v[222:223], 0, s[44:45]
	s_add_i32 s2, s3, s33
	global_load_lds_dwordx4 v[224:225], off
	v_lshl_add_u64 v[224:225], v[222:223], 0, v[198:199]
	s_mov_b32 m0, s2
	v_lshl_add_u64 v[222:223], v[222:223], 0, v[200:201]
	global_load_lds_dwordx4 v[224:225], off
	s_add_i32 m0, s2, 0x2000
	v_lshl_add_u64 v[194:195], v[194:195], 0, s[42:43]
	global_load_lds_dwordx4 v[222:223], off
	s_mov_b32 m0, s76
	s_and_b64 vcc, exec, s[62:63]
	global_load_lds_dwordx4 v[194:195], off
	v_lshl_add_u64 v[194:195], v[196:197], 0, s[42:43]
	s_mov_b32 m0, s77
	s_nop 0
	global_load_lds_dwordx4 v[194:195], off
	s_waitcnt vmcnt(8)
	s_waitcnt lgkmcnt(0)
	s_barrier
	s_cbranch_vccnz .LBB0_1399
	s_waitcnt lgkmcnt(0)
	v_mfma_f32_16x16x32_bf16 v[60:63], v[146:149], v[186:189], v[60:63]
	v_mfma_f32_16x16x32_bf16 v[56:59], v[154:157], v[186:189], v[56:59]
	v_mfma_f32_16x16x32_bf16 v[44:47], v[146:149], v[178:181], v[44:47]
	v_mfma_f32_16x16x32_bf16 v[40:43], v[154:157], v[178:181], v[40:43]
	v_mfma_f32_16x16x32_bf16 v[28:31], v[146:149], v[170:173], v[28:31]
	v_mfma_f32_16x16x32_bf16 v[24:27], v[154:157], v[170:173], v[24:27]
	v_mfma_f32_16x16x32_bf16 v[12:15], v[146:149], v[162:165], v[12:15]
	v_mfma_f32_16x16x32_bf16 v[8:11], v[154:157], v[162:165], v[8:11]
	v_mfma_f32_16x16x32_bf16 v[60:63], v[150:153], v[190:193], v[60:63]
	v_mfma_f32_16x16x32_bf16 v[56:59], v[158:161], v[190:193], v[56:59]
	v_mfma_f32_16x16x32_bf16 v[44:47], v[150:153], v[182:185], v[44:47]
	v_mfma_f32_16x16x32_bf16 v[40:43], v[158:161], v[182:185], v[40:43]
	v_mfma_f32_16x16x32_bf16 v[28:31], v[150:153], v[174:177], v[28:31]
	v_mfma_f32_16x16x32_bf16 v[24:27], v[158:161], v[174:177], v[24:27]
	v_mfma_f32_16x16x32_bf16 v[12:15], v[150:153], v[166:169], v[12:15]
	v_mfma_f32_16x16x32_bf16 v[8:11], v[158:161], v[166:169], v[8:11]
	v_mfma_f32_16x16x32_bf16 v[52:55], v[130:133], v[186:189], v[52:55]
	v_mfma_f32_16x16x32_bf16 v[48:51], v[138:141], v[186:189], v[48:51]
	v_mfma_f32_16x16x32_bf16 v[36:39], v[130:133], v[178:181], v[36:39]
	v_mfma_f32_16x16x32_bf16 v[32:35], v[138:141], v[178:181], v[32:35]
	v_mfma_f32_16x16x32_bf16 v[20:23], v[130:133], v[170:173], v[20:23]
	v_mfma_f32_16x16x32_bf16 v[16:19], v[138:141], v[170:173], v[16:19]
	v_mfma_f32_16x16x32_bf16 v[4:7], v[130:133], v[162:165], v[4:7]
	v_mfma_f32_16x16x32_bf16 v[0:3], v[138:141], v[162:165], v[0:3]
	v_mfma_f32_16x16x32_bf16 v[52:55], v[134:137], v[190:193], v[52:55]
	v_mfma_f32_16x16x32_bf16 v[48:51], v[142:145], v[190:193], v[48:51]
	v_mfma_f32_16x16x32_bf16 v[36:39], v[134:137], v[182:185], v[36:39]
	v_mfma_f32_16x16x32_bf16 v[32:35], v[142:145], v[182:185], v[32:35]
	v_mfma_f32_16x16x32_bf16 v[20:23], v[134:137], v[174:177], v[20:23]
	v_mfma_f32_16x16x32_bf16 v[16:19], v[142:145], v[174:177], v[16:19]
	v_mfma_f32_16x16x32_bf16 v[4:7], v[134:137], v[166:169], v[4:7]
	v_mfma_f32_16x16x32_bf16 v[0:3], v[142:145], v[166:169], v[0:3]
	s_branch .LBB0_1399

.LBB0_1443:
	s_lshl_b32 s72, s19, 7
	s_add_u32 s29, s76, s72
	s_addc_u32 s30, s77, 0
	s_add_u32 s22, s29, 0x100
	s_addc_u32 s23, s30, 0
	v_lshl_add_u64 v[144:145], v[142:143], 0, s[72:73]
	s_and_b64 s[2:3], s[60:61], exec
	v_lshl_add_u64 v[144:145], v[144:145], 0, s[46:47]
	s_cselect_b32 s23, s67, s23
	s_cselect_b32 s22, s66, s22
	v_cndmask_b32_e64 v145, v145, v141, s[60:61]
	v_cndmask_b32_e64 v144, v144, v140, s[60:61]
	s_add_i32 s60, 0, 0x10000
	v_add_u32_e32 v128, s60, v147
	s_add_i32 s61, 0, 0x14000
	ds_read_b128 v[150:153], v128
	ds_read_b128 v[154:157], v128 offset:1024
	ds_read_b128 v[158:161], v128 offset:2048
	ds_read_b128 v[162:165], v128 offset:3072
	v_add_u32_e32 v128, s61, v147
	ds_read_b128 v[166:169], v128
	ds_read_b128 v[170:173], v128 offset:1024
	ds_read_b128 v[174:177], v128 offset:2048
	ds_read_b128 v[178:181], v128 offset:3072
	s_add_u32 s2, s29, 0x20080
	s_addc_u32 s3, s30, 0
	v_lshl_add_u64 v[194:195], s[2:3], 0, v[130:131]
	s_add_i32 m0, s35, 0xc000
	ds_read_b128 v[182:185], v148
	ds_read_b128 v[186:189], v148 offset:1024
	ds_read_b128 v[190:193], v148 offset:2048
	ds_read_b128 v[198:201], v148 offset:3072
	ds_read_b128 v[202:205], v148 offset:4096
	ds_read_b128 v[206:209], v148 offset:5120
	ds_read_b128 v[210:213], v148 offset:6144
	ds_read_b128 v[214:217], v148 offset:7168
	global_load_lds_dwordx4 v[194:195], off
	v_lshl_add_u64 v[194:195], s[2:3], 0, v[134:135]
	s_add_i32 m0, s35, 0xe000
	s_nop 0
	global_load_lds_dwordx4 v[194:195], off
	s_waitcnt vmcnt(8)
	s_waitcnt lgkmcnt(0)
	s_barrier
	v_mfma_f32_16x16x32_bf16 v[124:127], v[150:153], v[182:185], v[124:127]
	v_mfma_f32_16x16x32_bf16 v[120:123], v[158:161], v[182:185], v[120:123]
	v_mfma_f32_16x16x32_bf16 v[112:115], v[150:153], v[190:193], v[112:115]
	v_mfma_f32_16x16x32_bf16 v[104:107], v[158:161], v[190:193], v[104:107]
	v_mfma_f32_16x16x32_bf16 v[96:99], v[150:153], v[202:205], v[96:99]
	v_mfma_f32_16x16x32_bf16 v[88:91], v[158:161], v[202:205], v[88:91]
	v_mfma_f32_16x16x32_bf16 v[80:83], v[150:153], v[210:213], v[80:83]
	v_mfma_f32_16x16x32_bf16 v[72:75], v[158:161], v[210:213], v[72:75]
	v_mfma_f32_16x16x32_bf16 v[124:127], v[154:157], v[186:189], v[124:127]
	v_mfma_f32_16x16x32_bf16 v[120:123], v[162:165], v[186:189], v[120:123]
	v_mfma_f32_16x16x32_bf16 v[112:115], v[154:157], v[198:201], v[112:115]
	v_mfma_f32_16x16x32_bf16 v[104:107], v[162:165], v[198:201], v[104:107]
	v_mfma_f32_16x16x32_bf16 v[96:99], v[154:157], v[206:209], v[96:99]
	v_mfma_f32_16x16x32_bf16 v[88:91], v[162:165], v[206:209], v[88:91]
	v_mfma_f32_16x16x32_bf16 v[80:83], v[154:157], v[214:217], v[80:83]
	v_mfma_f32_16x16x32_bf16 v[72:75], v[162:165], v[214:217], v[72:75]
	v_mfma_f32_16x16x32_bf16 v[116:119], v[166:169], v[182:185], v[116:119]
	v_mfma_f32_16x16x32_bf16 v[108:111], v[174:177], v[182:185], v[108:111]
	v_mfma_f32_16x16x32_bf16 v[100:103], v[166:169], v[190:193], v[100:103]
	v_mfma_f32_16x16x32_bf16 v[92:95], v[174:177], v[190:193], v[92:95]
	v_mfma_f32_16x16x32_bf16 v[84:87], v[166:169], v[202:205], v[84:87]
	v_mfma_f32_16x16x32_bf16 v[76:79], v[174:177], v[202:205], v[76:79]
	v_mfma_f32_16x16x32_bf16 v[68:71], v[166:169], v[210:213], v[68:71]
	v_mfma_f32_16x16x32_bf16 v[64:67], v[174:177], v[210:213], v[64:67]
	v_mfma_f32_16x16x32_bf16 v[116:119], v[170:173], v[186:189], v[116:119]
	v_mfma_f32_16x16x32_bf16 v[108:111], v[178:181], v[186:189], v[108:111]
	v_mfma_f32_16x16x32_bf16 v[100:103], v[170:173], v[198:201], v[100:103]
	v_mfma_f32_16x16x32_bf16 v[92:95], v[178:181], v[198:201], v[92:95]
	v_mfma_f32_16x16x32_bf16 v[84:87], v[170:173], v[206:209], v[84:87]
	v_mfma_f32_16x16x32_bf16 v[76:79], v[178:181], v[206:209], v[76:79]
	v_mfma_f32_16x16x32_bf16 v[68:71], v[170:173], v[214:217], v[68:71]
	v_mfma_f32_16x16x32_bf16 v[64:67], v[178:181], v[214:217], v[64:67]
	s_barrier
	s_add_i32 s2, s60, s33
	v_lshl_add_u64 v[194:195], v[144:145], 0, v[132:133]
	s_mov_b32 m0, s2
	ds_read_b128 v[182:185], v148 offset:16384
	ds_read_b128 v[186:189], v148 offset:17408
	ds_read_b128 v[190:193], v148 offset:18432
	ds_read_b128 v[198:201], v148 offset:19456
	ds_read_b128 v[202:205], v148 offset:20480
	ds_read_b128 v[206:209], v148 offset:21504
	ds_read_b128 v[210:213], v148 offset:22528
	ds_read_b128 v[214:217], v148 offset:23552
	global_load_lds_dwordx4 v[194:195], off
	v_lshl_add_u64 v[196:197], v[144:145], 0, v[136:137]
	s_add_i32 m0, s2, 0x2000
	v_lshl_add_u64 v[218:219], v[144:145], 0, s[48:49]
	s_add_i32 s2, s61, s33
	global_load_lds_dwordx4 v[196:197], off
	v_lshl_add_u64 v[220:221], v[218:219], 0, v[132:133]
	s_mov_b32 m0, s2
	v_lshl_add_u64 v[218:219], v[218:219], 0, v[136:137]
	global_load_lds_dwordx4 v[220:221], off
	s_add_i32 m0, s2, 0x2000
	v_lshl_add_u64 v[220:221], s[22:23], 0, v[134:135]
	global_load_lds_dwordx4 v[218:219], off
	v_lshl_add_u64 v[218:219], s[22:23], 0, v[130:131]
	s_mov_b32 m0, s35
	s_nop 0
	global_load_lds_dwordx4 v[218:219], off
	s_mov_b32 m0, s36
	s_nop 0
	global_load_lds_dwordx4 v[220:221], off
	s_waitcnt vmcnt(8)
	s_waitcnt lgkmcnt(0)
	s_barrier
	v_mfma_f32_16x16x32_bf16 v[60:63], v[150:153], v[182:185], v[60:63]
	v_mfma_f32_16x16x32_bf16 v[56:59], v[158:161], v[182:185], v[56:59]
	v_mfma_f32_16x16x32_bf16 v[48:51], v[150:153], v[190:193], v[48:51]
	v_mfma_f32_16x16x32_bf16 v[40:43], v[158:161], v[190:193], v[40:43]
	v_mfma_f32_16x16x32_bf16 v[32:35], v[150:153], v[202:205], v[32:35]
	v_mfma_f32_16x16x32_bf16 v[24:27], v[158:161], v[202:205], v[24:27]
	v_mfma_f32_16x16x32_bf16 v[16:19], v[150:153], v[210:213], v[16:19]
	v_mfma_f32_16x16x32_bf16 v[8:11], v[158:161], v[210:213], v[8:11]
	v_mfma_f32_16x16x32_bf16 v[60:63], v[154:157], v[186:189], v[60:63]
	v_mfma_f32_16x16x32_bf16 v[56:59], v[162:165], v[186:189], v[56:59]
	v_mfma_f32_16x16x32_bf16 v[48:51], v[154:157], v[198:201], v[48:51]
	v_mfma_f32_16x16x32_bf16 v[40:43], v[162:165], v[198:201], v[40:43]
	v_mfma_f32_16x16x32_bf16 v[32:35], v[154:157], v[206:209], v[32:35]
	v_mfma_f32_16x16x32_bf16 v[24:27], v[162:165], v[206:209], v[24:27]
	v_mfma_f32_16x16x32_bf16 v[16:19], v[154:157], v[214:217], v[16:19]
	v_mfma_f32_16x16x32_bf16 v[8:11], v[162:165], v[214:217], v[8:11]
	v_mfma_f32_16x16x32_bf16 v[52:55], v[166:169], v[182:185], v[52:55]
	v_mfma_f32_16x16x32_bf16 v[44:47], v[174:177], v[182:185], v[44:47]
	v_mfma_f32_16x16x32_bf16 v[36:39], v[166:169], v[190:193], v[36:39]
	v_mfma_f32_16x16x32_bf16 v[28:31], v[174:177], v[190:193], v[28:31]
	v_mfma_f32_16x16x32_bf16 v[20:23], v[166:169], v[202:205], v[20:23]
	v_mfma_f32_16x16x32_bf16 v[12:15], v[174:177], v[202:205], v[12:15]
	v_mfma_f32_16x16x32_bf16 v[4:7], v[166:169], v[210:213], v[4:7]
	v_mfma_f32_16x16x32_bf16 v[0:3], v[174:177], v[210:213], v[0:3]
	v_mfma_f32_16x16x32_bf16 v[52:55], v[170:173], v[186:189], v[52:55]
	v_mfma_f32_16x16x32_bf16 v[44:47], v[178:181], v[186:189], v[44:47]
	v_mfma_f32_16x16x32_bf16 v[36:39], v[170:173], v[198:201], v[36:39]
	v_mfma_f32_16x16x32_bf16 v[28:31], v[178:181], v[198:201], v[28:31]
	v_mfma_f32_16x16x32_bf16 v[20:23], v[170:173], v[206:209], v[20:23]
	v_mfma_f32_16x16x32_bf16 v[12:15], v[178:181], v[206:209], v[12:15]
	v_mfma_f32_16x16x32_bf16 v[4:7], v[170:173], v[214:217], v[4:7]
	v_mfma_f32_16x16x32_bf16 v[0:3], v[178:181], v[214:217], v[0:3]
	s_barrier
	s_add_i32 s29, 0, 0x18000
	v_add_u32_e32 v128, s29, v147
	s_add_i32 s30, 0, 0x1c000
	ds_read_b128 v[150:153], v128
	ds_read_b128 v[154:157], v128 offset:1024
	ds_read_b128 v[158:161], v128 offset:2048
	ds_read_b128 v[162:165], v128 offset:3072
	v_add_u32_e32 v128, s30, v147
	ds_read_b128 v[166:169], v128
	ds_read_b128 v[170:173], v128 offset:1024
	ds_read_b128 v[174:177], v128 offset:2048
	ds_read_b128 v[178:181], v128 offset:3072
	s_add_u32 s2, s22, 0x20000
	s_addc_u32 s3, s23, 0
	s_mov_b32 m0, s37
	v_lshl_add_u64 v[222:223], s[2:3], 0, v[130:131]
	ds_read_b128 v[182:185], v148 offset:32768
	ds_read_b128 v[186:189], v148 offset:33792
	ds_read_b128 v[190:193], v148 offset:34816
	ds_read_b128 v[198:201], v148 offset:35840
	ds_read_b128 v[202:205], v148 offset:36864
	ds_read_b128 v[206:209], v148 offset:37888
	ds_read_b128 v[210:213], v148 offset:38912
	ds_read_b128 v[214:217], v148 offset:39936
	global_load_lds_dwordx4 v[222:223], off
	v_lshl_add_u64 v[222:223], s[2:3], 0, v[134:135]
	s_mov_b32 m0, s38
	s_nop 0
	global_load_lds_dwordx4 v[222:223], off
	s_waitcnt vmcnt(8)
	s_waitcnt lgkmcnt(0)
	s_barrier
	v_mfma_f32_16x16x32_bf16 v[124:127], v[150:153], v[182:185], v[124:127]
	v_mfma_f32_16x16x32_bf16 v[120:123], v[158:161], v[182:185], v[120:123]
	v_mfma_f32_16x16x32_bf16 v[112:115], v[150:153], v[190:193], v[112:115]
	v_mfma_f32_16x16x32_bf16 v[104:107], v[158:161], v[190:193], v[104:107]
	v_mfma_f32_16x16x32_bf16 v[96:99], v[150:153], v[202:205], v[96:99]
	v_mfma_f32_16x16x32_bf16 v[88:91], v[158:161], v[202:205], v[88:91]
	v_mfma_f32_16x16x32_bf16 v[80:83], v[150:153], v[210:213], v[80:83]
	v_mfma_f32_16x16x32_bf16 v[72:75], v[158:161], v[210:213], v[72:75]
	v_mfma_f32_16x16x32_bf16 v[124:127], v[154:157], v[186:189], v[124:127]
	v_mfma_f32_16x16x32_bf16 v[120:123], v[162:165], v[186:189], v[120:123]
	v_mfma_f32_16x16x32_bf16 v[112:115], v[154:157], v[198:201], v[112:115]
	v_mfma_f32_16x16x32_bf16 v[104:107], v[162:165], v[198:201], v[104:107]
	v_mfma_f32_16x16x32_bf16 v[96:99], v[154:157], v[206:209], v[96:99]
	v_mfma_f32_16x16x32_bf16 v[88:91], v[162:165], v[206:209], v[88:91]
	v_mfma_f32_16x16x32_bf16 v[80:83], v[154:157], v[214:217], v[80:83]
	v_mfma_f32_16x16x32_bf16 v[72:75], v[162:165], v[214:217], v[72:75]
	v_mfma_f32_16x16x32_bf16 v[116:119], v[166:169], v[182:185], v[116:119]
	v_mfma_f32_16x16x32_bf16 v[108:111], v[174:177], v[182:185], v[108:111]
	v_mfma_f32_16x16x32_bf16 v[100:103], v[166:169], v[190:193], v[100:103]
	v_mfma_f32_16x16x32_bf16 v[92:95], v[174:177], v[190:193], v[92:95]
	v_mfma_f32_16x16x32_bf16 v[84:87], v[166:169], v[202:205], v[84:87]
	v_mfma_f32_16x16x32_bf16 v[76:79], v[174:177], v[202:205], v[76:79]
	v_mfma_f32_16x16x32_bf16 v[68:71], v[166:169], v[210:213], v[68:71]
	v_mfma_f32_16x16x32_bf16 v[64:67], v[174:177], v[210:213], v[64:67]
	v_mfma_f32_16x16x32_bf16 v[116:119], v[170:173], v[186:189], v[116:119]
	v_mfma_f32_16x16x32_bf16 v[108:111], v[178:181], v[186:189], v[108:111]
	v_mfma_f32_16x16x32_bf16 v[100:103], v[170:173], v[198:201], v[100:103]
	v_mfma_f32_16x16x32_bf16 v[92:95], v[178:181], v[198:201], v[92:95]
	v_mfma_f32_16x16x32_bf16 v[84:87], v[170:173], v[206:209], v[84:87]
	v_mfma_f32_16x16x32_bf16 v[76:79], v[178:181], v[206:209], v[76:79]
	v_mfma_f32_16x16x32_bf16 v[68:71], v[170:173], v[214:217], v[68:71]
	v_mfma_f32_16x16x32_bf16 v[64:67], v[178:181], v[214:217], v[64:67]
	s_barrier
	s_add_i32 s2, s29, s33
	v_lshl_add_u64 v[194:195], v[194:195], 0, s[42:43]
	s_mov_b32 m0, s2
	ds_read_b128 v[182:185], v148 offset:49152
	ds_read_b128 v[186:189], v148 offset:50176
	ds_read_b128 v[190:193], v148 offset:51200
	ds_read_b128 v[198:201], v148 offset:52224
	ds_read_b128 v[202:205], v148 offset:53248
	ds_read_b128 v[206:209], v148 offset:54272
	ds_read_b128 v[210:213], v148 offset:55296
	ds_read_b128 v[214:217], v148 offset:56320
	global_load_lds_dwordx4 v[194:195], off
	v_lshl_add_u64 v[194:195], v[196:197], 0, s[42:43]
	s_add_i32 m0, s2, 0x2000
	v_lshl_add_u64 v[144:145], v[144:145], 0, s[50:51]
	s_add_i32 s2, s30, s33
	global_load_lds_dwordx4 v[194:195], off
	v_lshl_add_u64 v[194:195], v[144:145], 0, v[132:133]
	s_mov_b32 m0, s2
	v_lshl_add_u64 v[144:145], v[144:145], 0, v[136:137]
	global_load_lds_dwordx4 v[194:195], off
	s_add_i32 m0, s2, 0x2000
	s_nop 0
	global_load_lds_dwordx4 v[144:145], off
	v_lshl_add_u64 v[144:145], v[218:219], 0, s[42:43]
	s_mov_b32 m0, s39
	s_nop 0
	global_load_lds_dwordx4 v[144:145], off
	v_lshl_add_u64 v[144:145], v[220:221], 0, s[42:43]
	s_mov_b32 m0, s53
	s_nop 0
	global_load_lds_dwordx4 v[144:145], off
	s_waitcnt vmcnt(8)
	s_waitcnt lgkmcnt(0)
	s_barrier
	v_mfma_f32_16x16x32_bf16 v[60:63], v[150:153], v[182:185], v[60:63]
	v_mfma_f32_16x16x32_bf16 v[56:59], v[158:161], v[182:185], v[56:59]
	v_mfma_f32_16x16x32_bf16 v[48:51], v[150:153], v[190:193], v[48:51]
	v_mfma_f32_16x16x32_bf16 v[40:43], v[158:161], v[190:193], v[40:43]
	v_mfma_f32_16x16x32_bf16 v[32:35], v[150:153], v[202:205], v[32:35]
	v_mfma_f32_16x16x32_bf16 v[24:27], v[158:161], v[202:205], v[24:27]
	v_mfma_f32_16x16x32_bf16 v[16:19], v[150:153], v[210:213], v[16:19]
	v_mfma_f32_16x16x32_bf16 v[8:11], v[158:161], v[210:213], v[8:11]
	v_mfma_f32_16x16x32_bf16 v[60:63], v[154:157], v[186:189], v[60:63]
	v_mfma_f32_16x16x32_bf16 v[56:59], v[162:165], v[186:189], v[56:59]
	v_mfma_f32_16x16x32_bf16 v[48:51], v[154:157], v[198:201], v[48:51]
	v_mfma_f32_16x16x32_bf16 v[40:43], v[162:165], v[198:201], v[40:43]
	v_mfma_f32_16x16x32_bf16 v[32:35], v[154:157], v[206:209], v[32:35]
	v_mfma_f32_16x16x32_bf16 v[24:27], v[162:165], v[206:209], v[24:27]
	v_mfma_f32_16x16x32_bf16 v[16:19], v[154:157], v[214:217], v[16:19]
	v_mfma_f32_16x16x32_bf16 v[8:11], v[162:165], v[214:217], v[8:11]
	v_mfma_f32_16x16x32_bf16 v[52:55], v[166:169], v[182:185], v[52:55]
	v_mfma_f32_16x16x32_bf16 v[44:47], v[174:177], v[182:185], v[44:47]
	v_mfma_f32_16x16x32_bf16 v[36:39], v[166:169], v[190:193], v[36:39]
	v_mfma_f32_16x16x32_bf16 v[28:31], v[174:177], v[190:193], v[28:31]
	v_mfma_f32_16x16x32_bf16 v[20:23], v[166:169], v[202:205], v[20:23]
	v_mfma_f32_16x16x32_bf16 v[12:15], v[174:177], v[202:205], v[12:15]
	v_mfma_f32_16x16x32_bf16 v[4:7], v[166:169], v[210:213], v[4:7]
	v_mfma_f32_16x16x32_bf16 v[0:3], v[174:177], v[210:213], v[0:3]
	v_mfma_f32_16x16x32_bf16 v[52:55], v[170:173], v[186:189], v[52:55]
	v_mfma_f32_16x16x32_bf16 v[44:47], v[178:181], v[186:189], v[44:47]
	v_mfma_f32_16x16x32_bf16 v[36:39], v[170:173], v[198:201], v[36:39]
	v_mfma_f32_16x16x32_bf16 v[28:31], v[178:181], v[198:201], v[28:31]
	v_mfma_f32_16x16x32_bf16 v[20:23], v[170:173], v[206:209], v[20:23]
	v_mfma_f32_16x16x32_bf16 v[12:15], v[178:181], v[206:209], v[12:15]
	v_mfma_f32_16x16x32_bf16 v[4:7], v[170:173], v[214:217], v[4:7]
	v_mfma_f32_16x16x32_bf16 v[0:3], v[178:181], v[214:217], v[0:3]
	s_barrier
	s_add_i32 s2, s19, 2
	s_cmp_gt_u32 s19, 5
	s_mov_b32 s19, s2
	s_cbranch_scc1 .LBB0_1450
